# LRU v7: v3 + L2 prefetch of the A tile two chunks ahead
# baseline (speedup 1.0000x reference)
.LBB0_1451:
	s_load_dwordx4 s[0:3], s[8:9], 0x138
	s_waitcnt lgkmcnt(0)
	s_mov_b64 s[4:5], s[0:1]
	s_cmp_lt_i32 s4, 12
	s_cselect_b64 s[0:1], -1, 0
	s_cmp_gt_i32 s5, 11
	s_cselect_b64 s[2:3], -1, 0
	s_and_b64 s[0:1], s[0:1], s[2:3]
	s_andn2_b64 vcc, exec, s[0:1]
	s_cbranch_vccnz .LBB0_1535
	s_mov_b64 s[24:25], s[8:9]
	v_mbcnt_lo_u32_b32 v202, -1, 0
	v_mbcnt_hi_u32_b32 v202, -1, v202
	s_load_dword s0, s[8:9], 0x148
	s_waitcnt lgkmcnt(0)
	v_writelane_b32 v241, s0, 18
	s_nop 1
	v_writelane_b32 v241, s1, 19
	s_add_u32 s0, s8, 0x148
	s_addc_u32 s1, s9, 0
	v_writelane_b32 v241, s0, 34
	s_nop 1
	v_writelane_b32 v241, s1, 35
	v_readlane_b32 s0, v243, 0
	s_cmpk_gt_i32 s0, 0xff
	v_readlane_b32 s1, v243, 1
	s_cbranch_scc1 .LBB0_1482
	v_readlane_b32 s0, v243, 7
	v_readlane_b32 s1, v243, 8
	v_readlane_b32 s4, v243, 0
	v_readlane_b32 s6, v243, 12
	s_load_dwordx2 s[2:3], s[0:1], 0x130
	s_lshr_b32 s7, s6, 2
	s_and_b32 s8, s6, 3
	s_bfe_u32 s11, s4, 0x20003
	s_lshr_b32 s50, s4, 5
	s_lshl_b32 s50, s50, 3
	s_and_b32 s51, s4, 7
	s_or_b32 s50, s50, s51
	s_lshr_b32 s9, s50, 2
	s_and_b32 s10, s50, 3
	v_and_b32_e32 v160, 15, v202
	v_lshrrev_b32_e32 v161, 4, v202
	v_lshlrev_b32_e32 v209, 2, v202
	s_lshl_b32 s50, s7, 15
	v_xor_b32_e32 v178, v161, v160
	v_lshlrev_b32_e32 v178, 4, v178
	v_lshl_add_u32 v162, v160, 9, v178
	v_add_u32_e32 v162, s50, v162
	s_lshl_b32 s51, s11, 6
	s_lshl_b32 s52, s8, 4
	s_add_i32 s51, s51, s52
	v_add_u32_e32 v179, s51, v160
	v_lshrrev_b32_e32 v180, 3, v179
	v_and_b32_e32 v181, 7, v179
	v_lshlrev_b32_e32 v181, 1, v181
	v_lshlrev_b32_e32 v182, 2, v161
	v_add_u32_e32 v183, 0, v182
	v_xor_b32_e32 v184, v180, v183
	v_lshlrev_b32_e32 v184, 4, v184
	v_lshl_add_u32 v184, v183, 9, v184
	v_add3_u32 v165, v184, v181, s50
	v_add_u32_e32 v183, 1, v182
	v_xor_b32_e32 v184, v180, v183
	v_lshlrev_b32_e32 v184, 4, v184
	v_lshl_add_u32 v184, v183, 9, v184
	v_add3_u32 v166, v184, v181, s50
	v_add_u32_e32 v183, 2, v182
	v_xor_b32_e32 v184, v180, v183
	v_lshlrev_b32_e32 v184, 4, v184
	v_lshl_add_u32 v184, v183, 9, v184
	v_add3_u32 v167, v184, v181, s50
	v_add_u32_e32 v183, 3, v182
	v_xor_b32_e32 v184, v180, v183
	v_lshlrev_b32_e32 v184, 4, v184
	v_lshl_add_u32 v184, v183, 9, v184
	v_add3_u32 v168, v184, v181, s50
	v_lshrrev_b32_e32 v185, 5, v202
	v_and_b32_e32 v186, 31, v202
	s_lshl_b32 s51, s6, 4
	v_add_u32_e32 v187, 0, v185
	v_xor_b32_e32 v188, v186, v187
	v_lshlrev_b32_e32 v188, 4, v188
	v_add_u32_e32 v187, s51, v187
	v_lshl_add_u32 v211, v187, 11, v188
	v_add_u32_e32 v187, 2, v185
	v_xor_b32_e32 v188, v186, v187
	v_lshlrev_b32_e32 v188, 4, v188
	v_add_u32_e32 v187, s51, v187
	v_lshl_add_u32 v212, v187, 11, v188
	v_add_u32_e32 v187, 4, v185
	v_xor_b32_e32 v188, v186, v187
	v_lshlrev_b32_e32 v188, 4, v188
	v_add_u32_e32 v187, s51, v187
	v_lshl_add_u32 v213, v187, 11, v188
	v_add_u32_e32 v187, 6, v185
	v_xor_b32_e32 v188, v186, v187
	v_lshlrev_b32_e32 v188, 4, v188
	v_add_u32_e32 v187, s51, v187
	v_lshl_add_u32 v214, v187, 11, v188
	v_add_u32_e32 v187, 8, v185
	v_xor_b32_e32 v188, v186, v187
	v_lshlrev_b32_e32 v188, 4, v188
	v_add_u32_e32 v187, s51, v187
	v_lshl_add_u32 v215, v187, 11, v188
	v_add_u32_e32 v187, 10, v185
	v_xor_b32_e32 v188, v186, v187
	v_lshlrev_b32_e32 v188, 4, v188
	v_add_u32_e32 v187, s51, v187
	v_lshl_add_u32 v216, v187, 11, v188
	v_add_u32_e32 v187, 12, v185
	v_xor_b32_e32 v188, v186, v187
	v_lshlrev_b32_e32 v188, 4, v188
	v_add_u32_e32 v187, s51, v187
	v_lshl_add_u32 v217, v187, 11, v188
	v_add_u32_e32 v187, 14, v185
	v_xor_b32_e32 v188, v186, v187
	v_lshlrev_b32_e32 v188, 4, v188
	v_add_u32_e32 v187, s51, v187
	v_lshl_add_u32 v218, v187, 11, v188
	v_lshrrev_b32_e32 v187, 3, v202
	v_and_b32_e32 v188, 7, v202
	v_lshrrev_b32_e32 v189, 2, v188
	v_lshl_add_u32 v187, v187, 1, v189
	s_lshl_b32 s51, s6, 4
	v_add_u32_e32 v187, s51, v187
	v_and_b32_e32 v188, 3, v188
	v_lshlrev_b32_e32 v188, 7, v188
	v_lshl_add_u32 v169, v187, 11, v188
	s_lshl_b32 s51, s6, 7
	s_add_i32 s51, s51, 0x20000
	v_lshl_add_u32 v207, v160, 3, s51
	s_lshl_b32 s51, s8, 7
	s_add_i32 s51, s51, 0x20000
	v_lshl_add_u32 v208, v160, 3, s51
	s_lshl_b32 s51, s7, 6
	v_add_u32_e32 v189, s51, v182
	s_lshl_b32 s51, s8, 4
	v_add_u32_e32 v190, s51, v160
	v_lshlrev_b32_e32 v190, 1, v190
	v_lshl_add_u32 v210, v189, 11, v190
	s_waitcnt lgkmcnt(0)
	s_lshl_b32 s50, s10, 9
	s_add_u32 s16, s2, s50
	s_addc_u32 s17, s3, 0
	s_add_u32 s16, s16, 0x1b900000
	s_addc_u32 s17, s17, 0
	s_lshl_b32 s50, s10, 9
	s_lshl_b32 s51, s11, 7
	s_add_i32 s50, s50, s51
	s_add_u32 s18, s2, s50
	s_addc_u32 s19, s3, 0
	s_add_u32 s18, s18, 0x13100000
	s_addc_u32 s19, s19, 0
	s_add_u32 s20, s2, s50
	s_addc_u32 s21, s3, 0
	s_add_u32 s20, s20, 0x29100000
	s_addc_u32 s21, s21, 0
	s_lshl_b32 s50, s4, 18
	s_add_u32 s22, s2, s50
	s_addc_u32 s23, s3, 0
	s_add_u32 s22, s22, 0x20100000
	s_addc_u32 s23, s23, 0
	s_lshl_b32 s50, s10, 10
	s_lshl_b32 s51, s11, 6
	s_add_i32 s50, s50, s51
	s_lshl_b32 s51, s8, 4
	s_add_i32 s50, s50, s51
	s_add_i32 s50, s50, 0
	s_lshl_b32 s50, s50, 9
	s_add_u32 s46, s2, s50
	s_addc_u32 s47, s3, 0
	s_add_u32 s46, s46, 0x1000000
	s_addc_u32 s47, s47, 0
	s_add_u32 s48, s46, 0x20000
	s_addc_u32 s49, s47, 0
	v_lshlrev_b32_e32 v178, 9, v160
	v_lshl_add_u32 v178, v161, 4, v178
	global_load_dwordx4 v[0:3], v178, s[46:47]
	global_load_dwordx4 v[4:7], v178, s[46:47] offset:64
	global_load_dwordx4 v[8:11], v178, s[46:47] offset:128
	global_load_dwordx4 v[12:15], v178, s[46:47] offset:192
	global_load_dwordx4 v[16:19], v178, s[46:47] offset:256
	global_load_dwordx4 v[20:23], v178, s[46:47] offset:320
	global_load_dwordx4 v[24:27], v178, s[46:47] offset:384
	global_load_dwordx4 v[28:31], v178, s[46:47] offset:448
	global_load_dwordx4 v[32:35], v178, s[48:49]
	global_load_dwordx4 v[36:39], v178, s[48:49] offset:64
	global_load_dwordx4 v[40:43], v178, s[48:49] offset:128
	global_load_dwordx4 v[44:47], v178, s[48:49] offset:192
	global_load_dwordx4 v[48:51], v178, s[48:49] offset:256
	global_load_dwordx4 v[52:55], v178, s[48:49] offset:320
	global_load_dwordx4 v[56:59], v178, s[48:49] offset:384
	global_load_dwordx4 v[60:63], v178, s[48:49] offset:448
	s_load_dwordx2 s[46:47], s[0:1], 0xa0
	s_load_dwordx2 s[48:49], s[0:1], 0xb0
	s_load_dwordx2 s[40:41], s[0:1], 0xb8
	s_lshl_b32 s50, s10, 8
	s_lshl_b32 s51, s11, 6
	s_add_i32 s50, s50, s51
	s_lshl_b32 s51, s8, 4
	s_add_i32 s50, s50, s51
	v_add_u32_e32 v179, s50, v160
	v_lshlrev_b32_e32 v179, 2, v179
	s_waitcnt lgkmcnt(0)
	global_load_dword v173, v179, s[46:47]
	global_load_dword v174, v179, s[48:49]
	global_load_dword v175, v179, s[40:41]
	v_cmp_le_u32_e64 s[34:35], 16, v202
	v_cmp_le_u32_e64 s[36:37], 32, v202
	v_add_u32_e32 v204, -16, v202
	v_add_u32_e32 v205, -32, v202
	v_add_u32_e32 v206, 48, v160
	s_cmp_eq_u32 s7, 1
	s_cselect_b64 s[38:39], -1, 0
	v_and_b32_e32 v204, 63, v204
	v_lshlrev_b32_e32 v204, 2, v204
	v_and_b32_e32 v205, 63, v205
	v_lshlrev_b32_e32 v205, 2, v205
	v_and_b32_e32 v206, 63, v206
	v_lshlrev_b32_e32 v206, 2, v206
	v_mov_b32_e32 v176, 0
	s_mov_b32 s53, 0xbfb8aa3b
	s_waitcnt vmcnt(0)
	v_mul_f32_e32 v173, s53, v173
	v_mul_f32_e32 v174, s53, v174
	v_mul_f32_e32 v175, s53, v175
	v_exp_f32_e32 v175, v175
	s_nop 0
	v_add_f32_e32 v180, 1.0, v175
	v_log_f32_e32 v180, v180
	v_mov_b32_e32 v181, 0x3eaaaaab
	v_fma_f32 v181, v175, v181, -0.5
	v_fma_f32 v181, v175, v181, 1.0
	v_mul_f32_e32 v181, v175, v181
	v_mul_f32_e32 v181, 0x3fb8aa3b, v181
	v_cmp_gt_f32_e32 vcc, 0x3cf5c28f, v175
	s_nop 1
	v_cndmask_b32_e32 v175, v180, v181, vcc
	v_mul_f32_e32 v175, 0xc1000000, v175
	s_mov_b32 s13, 0
	s_barrier
	s_cmp_lt_u32 s13, 2
	s_lshl_b32 s50, s13, 7
	s_lshl_b32 s51, s9, 8
	s_add_i32 s51, s51, 0x8000
	s_add_i32 s51, s51, s50
	s_lshl_b32 s59, s9, 11
	s_add_i32 s59, s59, s50
	s_addk_i32 s59, 0xff00
	s_cmp_lt_u32 s13, 2
	s_cselect_b32 s59, s51, s59
	s_lshl_b32 s52, s59, 11
	s_add_u32 s46, s16, s52
	s_addc_u32 s47, s17, 0
	s_lshl_b32 s52, s6, 13
	s_mov_b32 m0, s52
	s_add_i32 s52, s52, 0x400
	global_load_lds_dwordx4 v211, s[46:47]
	s_mov_b32 m0, s52
	s_add_i32 s52, s52, 0x400
	global_load_lds_dwordx4 v212, s[46:47]
	s_mov_b32 m0, s52
	s_add_i32 s52, s52, 0x400
	global_load_lds_dwordx4 v213, s[46:47]
	s_mov_b32 m0, s52
	s_add_i32 s52, s52, 0x400
	global_load_lds_dwordx4 v214, s[46:47]
	s_mov_b32 m0, s52
	s_add_i32 s52, s52, 0x400
	global_load_lds_dwordx4 v215, s[46:47]
	s_mov_b32 m0, s52
	s_add_i32 s52, s52, 0x400
	global_load_lds_dwordx4 v216, s[46:47]
	s_mov_b32 m0, s52
	s_add_i32 s52, s52, 0x400
	global_load_lds_dwordx4 v217, s[46:47]
	s_mov_b32 m0, s52
	s_nop 0
	global_load_lds_dwordx4 v218, s[46:47]
	s_waitcnt vmcnt(0)
	s_barrier
	s_cmp_gt_u32 s13, 15
	s_cbranch_scc1 .Lmylru_nopf_1
	s_add_i32 s58, s13, 2
	s_cmp_lt_u32 s58, 2
	s_lshl_b32 s50, s58, 7
	s_lshl_b32 s51, s9, 8
	s_add_i32 s51, s51, 0x8000
	s_add_i32 s51, s51, s50
	s_lshl_b32 s59, s9, 11
	s_add_i32 s59, s59, s50
	s_addk_i32 s59, 0xff00
	s_cmp_lt_u32 s58, 2
	s_cselect_b32 s59, s51, s59
	s_lshl_b32 s52, s59, 11
	s_add_u32 s46, s16, s52
	s_addc_u32 s47, s17, 0
	s_lshl_b32 s52, s6, 10
	s_add_i32 s52, s52, 0x24800
	s_mov_b32 m0, s52
	s_nop 0
	global_load_lds_dwordx4 v169, s[46:47]
.Lmylru_nopf_1:
	s_cmp_eq_u32 s13, 17
	s_cbranch_scc1 .Lmylru_nodma_1
	s_add_i32 s58, s13, 1
	s_cmp_lt_u32 s58, 2
	s_lshl_b32 s50, s58, 7
	s_lshl_b32 s51, s9, 8
	s_add_i32 s51, s51, 0x8000
	s_add_i32 s51, s51, s50
	s_lshl_b32 s59, s9, 11
	s_add_i32 s59, s59, s50
	s_addk_i32 s59, 0xff00
	s_cmp_lt_u32 s58, 2
	s_cselect_b32 s59, s51, s59
	s_lshl_b32 s52, s59, 11
	s_add_u32 s46, s16, s52
	s_addc_u32 s47, s17, 0
	s_lshl_b32 s52, s6, 13
	s_add_i32 s52, s52, 0x10000
	s_mov_b32 m0, s52
	s_add_i32 s52, s52, 0x400
	global_load_lds_dwordx4 v211, s[46:47]
	s_mov_b32 m0, s52
	s_add_i32 s52, s52, 0x400
	global_load_lds_dwordx4 v212, s[46:47]
	s_mov_b32 m0, s52
	s_add_i32 s52, s52, 0x400
	global_load_lds_dwordx4 v213, s[46:47]
	s_mov_b32 m0, s52
	s_add_i32 s52, s52, 0x400
	global_load_lds_dwordx4 v214, s[46:47]
	s_mov_b32 m0, s52
	s_add_i32 s52, s52, 0x400
	global_load_lds_dwordx4 v215, s[46:47]
	s_mov_b32 m0, s52
	s_add_i32 s52, s52, 0x400
	global_load_lds_dwordx4 v216, s[46:47]
	s_mov_b32 m0, s52
	s_add_i32 s52, s52, 0x400
	global_load_lds_dwordx4 v217, s[46:47]
	s_mov_b32 m0, s52
	s_nop 0
	global_load_lds_dwordx4 v218, s[46:47]
.Lmylru_nodma_1:
	v_mov_b32_e32 v163, v162
	ds_read_b128 v[96:99], v163
	ds_read_b128 v[100:103], v163 offset:8192
	ds_read_b128 v[104:107], v163 offset:16384
	ds_read_b128 v[108:111], v163 offset:24576
	v_xor_b32_e32 v164, 0x40, v163
	ds_read_b128 v[112:115], v164
	ds_read_b128 v[116:119], v164 offset:8192
	ds_read_b128 v[120:123], v164 offset:16384
	ds_read_b128 v[124:127], v164 offset:24576
	s_waitcnt lgkmcnt(7)
	v_mfma_f32_16x16x32_bf16 v[64:67], v[96:99], v[0:3], 0
	v_mfma_f32_16x16x32_bf16 v[68:71], v[96:99], v[32:35], 0
	v_xor_b32_e32 v164, 0x80, v163
	ds_read_b128 v[96:99], v164
	s_waitcnt lgkmcnt(7)
	v_mfma_f32_16x16x32_bf16 v[72:75], v[100:103], v[0:3], 0
	v_mfma_f32_16x16x32_bf16 v[76:79], v[100:103], v[32:35], 0
	ds_read_b128 v[100:103], v164 offset:8192
	s_waitcnt lgkmcnt(7)
	v_mfma_f32_16x16x32_bf16 v[80:83], v[104:107], v[0:3], 0
	v_mfma_f32_16x16x32_bf16 v[84:87], v[104:107], v[32:35], 0
	ds_read_b128 v[104:107], v164 offset:16384
	s_waitcnt lgkmcnt(7)
	v_mfma_f32_16x16x32_bf16 v[88:91], v[108:111], v[0:3], 0
	v_mfma_f32_16x16x32_bf16 v[92:95], v[108:111], v[32:35], 0
	ds_read_b128 v[108:111], v164 offset:24576
	s_waitcnt lgkmcnt(7)
	v_mfma_f32_16x16x32_bf16 v[64:67], v[112:115], v[4:7], v[64:67]
	v_mfma_f32_16x16x32_bf16 v[68:71], v[112:115], v[36:39], v[68:71]
	v_xor_b32_e32 v164, 0xc0, v163
	ds_read_b128 v[112:115], v164
	s_waitcnt lgkmcnt(7)
	v_mfma_f32_16x16x32_bf16 v[72:75], v[116:119], v[4:7], v[72:75]
	v_mfma_f32_16x16x32_bf16 v[76:79], v[116:119], v[36:39], v[76:79]
	ds_read_b128 v[116:119], v164 offset:8192
	s_waitcnt lgkmcnt(7)
	v_mfma_f32_16x16x32_bf16 v[80:83], v[120:123], v[4:7], v[80:83]
	v_mfma_f32_16x16x32_bf16 v[84:87], v[120:123], v[36:39], v[84:87]
	ds_read_b128 v[120:123], v164 offset:16384
	s_waitcnt lgkmcnt(7)
	v_mfma_f32_16x16x32_bf16 v[88:91], v[124:127], v[4:7], v[88:91]
	v_mfma_f32_16x16x32_bf16 v[92:95], v[124:127], v[36:39], v[92:95]
	ds_read_b128 v[124:127], v164 offset:24576
	s_waitcnt lgkmcnt(7)
	v_mfma_f32_16x16x32_bf16 v[64:67], v[96:99], v[8:11], v[64:67]
	v_mfma_f32_16x16x32_bf16 v[68:71], v[96:99], v[40:43], v[68:71]
	v_xor_b32_e32 v164, 0x100, v163
	ds_read_b128 v[96:99], v164
	s_waitcnt lgkmcnt(7)
	v_mfma_f32_16x16x32_bf16 v[72:75], v[100:103], v[8:11], v[72:75]
	v_mfma_f32_16x16x32_bf16 v[76:79], v[100:103], v[40:43], v[76:79]
	ds_read_b128 v[100:103], v164 offset:8192
	s_waitcnt lgkmcnt(7)
	v_mfma_f32_16x16x32_bf16 v[80:83], v[104:107], v[8:11], v[80:83]
	v_mfma_f32_16x16x32_bf16 v[84:87], v[104:107], v[40:43], v[84:87]
	ds_read_b128 v[104:107], v164 offset:16384
	s_waitcnt lgkmcnt(7)
	v_mfma_f32_16x16x32_bf16 v[88:91], v[108:111], v[8:11], v[88:91]
	v_mfma_f32_16x16x32_bf16 v[92:95], v[108:111], v[40:43], v[92:95]
	ds_read_b128 v[108:111], v164 offset:24576
	s_waitcnt lgkmcnt(7)
	v_mfma_f32_16x16x32_bf16 v[64:67], v[112:115], v[12:15], v[64:67]
	v_mfma_f32_16x16x32_bf16 v[68:71], v[112:115], v[44:47], v[68:71]
	v_xor_b32_e32 v164, 0x140, v163
	ds_read_b128 v[112:115], v164
	s_waitcnt lgkmcnt(7)
	v_mfma_f32_16x16x32_bf16 v[72:75], v[116:119], v[12:15], v[72:75]
	v_mfma_f32_16x16x32_bf16 v[76:79], v[116:119], v[44:47], v[76:79]
	ds_read_b128 v[116:119], v164 offset:8192
	s_waitcnt lgkmcnt(7)
	v_mfma_f32_16x16x32_bf16 v[80:83], v[120:123], v[12:15], v[80:83]
	v_mfma_f32_16x16x32_bf16 v[84:87], v[120:123], v[44:47], v[84:87]
	ds_read_b128 v[120:123], v164 offset:16384
	s_waitcnt lgkmcnt(7)
	v_mfma_f32_16x16x32_bf16 v[88:91], v[124:127], v[12:15], v[88:91]
	v_mfma_f32_16x16x32_bf16 v[92:95], v[124:127], v[44:47], v[92:95]
	ds_read_b128 v[124:127], v164 offset:24576
	s_waitcnt lgkmcnt(7)
	v_mfma_f32_16x16x32_bf16 v[64:67], v[96:99], v[16:19], v[64:67]
	v_mfma_f32_16x16x32_bf16 v[68:71], v[96:99], v[48:51], v[68:71]
	v_xor_b32_e32 v164, 0x180, v163
	ds_read_b128 v[96:99], v164
	s_waitcnt lgkmcnt(7)
	v_mfma_f32_16x16x32_bf16 v[72:75], v[100:103], v[16:19], v[72:75]
	v_mfma_f32_16x16x32_bf16 v[76:79], v[100:103], v[48:51], v[76:79]
	ds_read_b128 v[100:103], v164 offset:8192
	s_waitcnt lgkmcnt(7)
	v_mfma_f32_16x16x32_bf16 v[80:83], v[104:107], v[16:19], v[80:83]
	v_mfma_f32_16x16x32_bf16 v[84:87], v[104:107], v[48:51], v[84:87]
	ds_read_b128 v[104:107], v164 offset:16384
	s_waitcnt lgkmcnt(7)
	v_mfma_f32_16x16x32_bf16 v[88:91], v[108:111], v[16:19], v[88:91]
	v_mfma_f32_16x16x32_bf16 v[92:95], v[108:111], v[48:51], v[92:95]
	ds_read_b128 v[108:111], v164 offset:24576
	s_waitcnt lgkmcnt(7)
	v_mfma_f32_16x16x32_bf16 v[64:67], v[112:115], v[20:23], v[64:67]
	v_mfma_f32_16x16x32_bf16 v[68:71], v[112:115], v[52:55], v[68:71]
	v_xor_b32_e32 v164, 0x1c0, v163
	ds_read_b128 v[112:115], v164
	s_waitcnt lgkmcnt(7)
	v_mfma_f32_16x16x32_bf16 v[72:75], v[116:119], v[20:23], v[72:75]
	v_mfma_f32_16x16x32_bf16 v[76:79], v[116:119], v[52:55], v[76:79]
	ds_read_b128 v[116:119], v164 offset:8192
	s_waitcnt lgkmcnt(7)
	v_mfma_f32_16x16x32_bf16 v[80:83], v[120:123], v[20:23], v[80:83]
	v_mfma_f32_16x16x32_bf16 v[84:87], v[120:123], v[52:55], v[84:87]
	ds_read_b128 v[120:123], v164 offset:16384
	s_waitcnt lgkmcnt(7)
	v_mfma_f32_16x16x32_bf16 v[88:91], v[124:127], v[20:23], v[88:91]
	v_mfma_f32_16x16x32_bf16 v[92:95], v[124:127], v[52:55], v[92:95]
	ds_read_b128 v[124:127], v164 offset:24576
	s_waitcnt lgkmcnt(7)
	v_mfma_f32_16x16x32_bf16 v[64:67], v[96:99], v[24:27], v[64:67]
	v_mfma_f32_16x16x32_bf16 v[68:71], v[96:99], v[56:59], v[68:71]
	s_waitcnt lgkmcnt(6)
	v_mfma_f32_16x16x32_bf16 v[72:75], v[100:103], v[24:27], v[72:75]
	v_mfma_f32_16x16x32_bf16 v[76:79], v[100:103], v[56:59], v[76:79]
	s_waitcnt lgkmcnt(5)
	v_mfma_f32_16x16x32_bf16 v[80:83], v[104:107], v[24:27], v[80:83]
	v_mfma_f32_16x16x32_bf16 v[84:87], v[104:107], v[56:59], v[84:87]
	s_waitcnt lgkmcnt(4)
	v_mfma_f32_16x16x32_bf16 v[88:91], v[108:111], v[24:27], v[88:91]
	v_mfma_f32_16x16x32_bf16 v[92:95], v[108:111], v[56:59], v[92:95]
	s_waitcnt lgkmcnt(3)
	v_mfma_f32_16x16x32_bf16 v[64:67], v[112:115], v[28:31], v[64:67]
	v_mfma_f32_16x16x32_bf16 v[68:71], v[112:115], v[60:63], v[68:71]
	s_waitcnt lgkmcnt(2)
	v_mfma_f32_16x16x32_bf16 v[72:75], v[116:119], v[28:31], v[72:75]
	v_mfma_f32_16x16x32_bf16 v[76:79], v[116:119], v[60:63], v[76:79]
	s_waitcnt lgkmcnt(1)
	v_mfma_f32_16x16x32_bf16 v[80:83], v[120:123], v[28:31], v[80:83]
	v_mfma_f32_16x16x32_bf16 v[84:87], v[120:123], v[60:63], v[84:87]
	s_waitcnt lgkmcnt(0)
	v_mfma_f32_16x16x32_bf16 v[88:91], v[124:127], v[28:31], v[88:91]
	v_mfma_f32_16x16x32_bf16 v[92:95], v[124:127], v[60:63], v[92:95]
	v_mov_b32_e32 v198, v165
	v_mov_b32_e32 v199, v166
	v_mov_b32_e32 v200, v167
	v_mov_b32_e32 v201, v168
	ds_read_u16 v144, v198
	ds_read_u16 v145, v199
	ds_read_u16 v146, v200
	ds_read_u16 v147, v201
	ds_read_u16 v148, v198 offset:8192
	ds_read_u16 v149, v199 offset:8192
	ds_read_u16 v150, v200 offset:8192
	ds_read_u16 v151, v201 offset:8192
	ds_read_u16 v152, v198 offset:16384
	ds_read_u16 v153, v199 offset:16384
	ds_read_u16 v154, v200 offset:16384
	ds_read_u16 v155, v201 offset:16384
	ds_read_u16 v156, v198 offset:24576
	ds_read_u16 v157, v199 offset:24576
	ds_read_u16 v158, v200 offset:24576
	ds_read_u16 v159, v201 offset:24576
	s_nop 7
	v_fma_f32 v178, v64, s53, v173
	v_fma_f32 v179, v65, s53, v173
	v_fma_f32 v180, v66, s53, v173
	v_fma_f32 v181, v67, s53, v173
	v_fma_f32 v182, v72, s53, v173
	v_fma_f32 v183, v73, s53, v173
	v_fma_f32 v184, v74, s53, v173
	v_fma_f32 v185, v75, s53, v173
	v_fma_f32 v186, v68, s53, v174
	v_fma_f32 v187, v69, s53, v174
	v_fma_f32 v188, v70, s53, v174
	v_fma_f32 v189, v71, s53, v174
	v_fma_f32 v190, v76, s53, v174
	v_fma_f32 v191, v77, s53, v174
	v_fma_f32 v192, v78, s53, v174
	v_fma_f32 v193, v79, s53, v174
	v_exp_f32_e32 v178, v178
	v_exp_f32_e32 v179, v179
	v_exp_f32_e32 v180, v180
	v_exp_f32_e32 v181, v181
	v_exp_f32_e32 v182, v182
	v_exp_f32_e32 v183, v183
	v_exp_f32_e32 v184, v184
	v_exp_f32_e32 v185, v185
	v_exp_f32_e32 v186, v186
	v_exp_f32_e32 v187, v187
	v_exp_f32_e32 v188, v188
	v_exp_f32_e32 v189, v189
	v_exp_f32_e32 v190, v190
	v_exp_f32_e32 v191, v191
	v_exp_f32_e32 v192, v192
	v_exp_f32_e32 v193, v193
	v_add_f32_e32 v178, 1.0, v178
	v_add_f32_e32 v179, 1.0, v179
	v_add_f32_e32 v180, 1.0, v180
	v_add_f32_e32 v181, 1.0, v181
	v_add_f32_e32 v182, 1.0, v182
	v_add_f32_e32 v183, 1.0, v183
	v_add_f32_e32 v184, 1.0, v184
	v_add_f32_e32 v185, 1.0, v185
	v_add_f32_e32 v186, 1.0, v186
	v_add_f32_e32 v187, 1.0, v187
	v_add_f32_e32 v188, 1.0, v188
	v_add_f32_e32 v189, 1.0, v189
	v_add_f32_e32 v190, 1.0, v190
	v_add_f32_e32 v191, 1.0, v191
	v_add_f32_e32 v192, 1.0, v192
	v_add_f32_e32 v193, 1.0, v193
	v_rcp_f32_e32 v178, v178
	v_rcp_f32_e32 v179, v179
	v_rcp_f32_e32 v180, v180
	v_rcp_f32_e32 v181, v181
	v_rcp_f32_e32 v182, v182
	v_rcp_f32_e32 v183, v183
	v_rcp_f32_e32 v184, v184
	v_rcp_f32_e32 v185, v185
	v_rcp_f32_e32 v186, v186
	v_rcp_f32_e32 v187, v187
	v_rcp_f32_e32 v188, v188
	v_rcp_f32_e32 v189, v189
	v_rcp_f32_e32 v190, v190
	v_rcp_f32_e32 v191, v191
	v_rcp_f32_e32 v192, v192
	v_rcp_f32_e32 v193, v193
	v_mul_f32_e32 v178, v175, v178
	v_mul_f32_e32 v179, v175, v179
	v_mul_f32_e32 v180, v175, v180
	v_mul_f32_e32 v181, v175, v181
	v_mul_f32_e32 v182, v175, v182
	v_mul_f32_e32 v183, v175, v183
	v_mul_f32_e32 v184, v175, v184
	v_mul_f32_e32 v185, v175, v185
	v_exp_f32_e32 v96, v178
	v_exp_f32_e32 v97, v179
	v_exp_f32_e32 v98, v180
	v_exp_f32_e32 v99, v181
	v_exp_f32_e32 v100, v182
	v_exp_f32_e32 v101, v183
	v_exp_f32_e32 v102, v184
	v_exp_f32_e32 v103, v185
	s_nop 0
	v_fma_f32 v194, -v96, v96, 1.0
	v_fma_f32 v195, -v97, v97, 1.0
	v_fma_f32 v196, -v98, v98, 1.0
	v_fma_f32 v197, -v99, v99, 1.0
	v_fma_f32 v198, -v100, v100, 1.0
	v_fma_f32 v199, -v101, v101, 1.0
	v_fma_f32 v200, -v102, v102, 1.0
	v_fma_f32 v201, -v103, v103, 1.0
	v_max_f32_e32 v194, 0, v194
	v_max_f32_e32 v195, 0, v195
	v_max_f32_e32 v196, 0, v196
	v_max_f32_e32 v197, 0, v197
	v_max_f32_e32 v198, 0, v198
	v_max_f32_e32 v199, 0, v199
	v_max_f32_e32 v200, 0, v200
	v_max_f32_e32 v201, 0, v201
	v_sqrt_f32_e32 v194, v194
	v_sqrt_f32_e32 v195, v195
	v_sqrt_f32_e32 v196, v196
	v_sqrt_f32_e32 v197, v197
	v_sqrt_f32_e32 v198, v198
	v_sqrt_f32_e32 v199, v199
	v_sqrt_f32_e32 v200, v200
	v_sqrt_f32_e32 v201, v201
	s_waitcnt lgkmcnt(8)
	v_lshlrev_b32_e32 v144, 16, v144
	v_lshlrev_b32_e32 v145, 16, v145
	v_lshlrev_b32_e32 v146, 16, v146
	v_lshlrev_b32_e32 v147, 16, v147
	v_lshlrev_b32_e32 v148, 16, v148
	v_lshlrev_b32_e32 v149, 16, v149
	v_lshlrev_b32_e32 v150, 16, v150
	v_lshlrev_b32_e32 v151, 16, v151
	v_mul_f32_e32 v194, v194, v186
	v_mul_f32_e32 v195, v195, v187
	v_mul_f32_e32 v196, v196, v188
	v_mul_f32_e32 v197, v197, v189
	v_mul_f32_e32 v198, v198, v190
	v_mul_f32_e32 v199, v199, v191
	v_mul_f32_e32 v200, v200, v192
	v_mul_f32_e32 v201, v201, v193
	v_mul_f32_e32 v144, v194, v144
	v_mul_f32_e32 v145, v195, v145
	v_mul_f32_e32 v146, v196, v146
	v_mul_f32_e32 v147, v197, v147
	v_mul_f32_e32 v148, v198, v148
	v_mul_f32_e32 v149, v199, v149
	v_mul_f32_e32 v150, v200, v150
	v_mul_f32_e32 v151, v201, v151
	v_fma_f32 v178, v80, s53, v173
	v_fma_f32 v179, v81, s53, v173
	v_fma_f32 v180, v82, s53, v173
	v_fma_f32 v181, v83, s53, v173
	v_fma_f32 v182, v88, s53, v173
	v_fma_f32 v183, v89, s53, v173
	v_fma_f32 v184, v90, s53, v173
	v_fma_f32 v185, v91, s53, v173
	v_fma_f32 v186, v84, s53, v174
	v_fma_f32 v187, v85, s53, v174
	v_fma_f32 v188, v86, s53, v174
	v_fma_f32 v189, v87, s53, v174
	v_fma_f32 v190, v92, s53, v174
	v_fma_f32 v191, v93, s53, v174
	v_fma_f32 v192, v94, s53, v174
	v_fma_f32 v193, v95, s53, v174
	v_exp_f32_e32 v178, v178
	v_exp_f32_e32 v179, v179
	v_exp_f32_e32 v180, v180
	v_exp_f32_e32 v181, v181
	v_exp_f32_e32 v182, v182
	v_exp_f32_e32 v183, v183
	v_exp_f32_e32 v184, v184
	v_exp_f32_e32 v185, v185
	v_exp_f32_e32 v186, v186
	v_exp_f32_e32 v187, v187
	v_exp_f32_e32 v188, v188
	v_exp_f32_e32 v189, v189
	v_exp_f32_e32 v190, v190
	v_exp_f32_e32 v191, v191
	v_exp_f32_e32 v192, v192
	v_exp_f32_e32 v193, v193
	v_add_f32_e32 v178, 1.0, v178
	v_add_f32_e32 v179, 1.0, v179
	v_add_f32_e32 v180, 1.0, v180
	v_add_f32_e32 v181, 1.0, v181
	v_add_f32_e32 v182, 1.0, v182
	v_add_f32_e32 v183, 1.0, v183
	v_add_f32_e32 v184, 1.0, v184
	v_add_f32_e32 v185, 1.0, v185
	v_add_f32_e32 v186, 1.0, v186
	v_add_f32_e32 v187, 1.0, v187
	v_add_f32_e32 v188, 1.0, v188
	v_add_f32_e32 v189, 1.0, v189
	v_add_f32_e32 v190, 1.0, v190
	v_add_f32_e32 v191, 1.0, v191
	v_add_f32_e32 v192, 1.0, v192
	v_add_f32_e32 v193, 1.0, v193
	v_rcp_f32_e32 v178, v178
	v_rcp_f32_e32 v179, v179
	v_rcp_f32_e32 v180, v180
	v_rcp_f32_e32 v181, v181
	v_rcp_f32_e32 v182, v182
	v_rcp_f32_e32 v183, v183
	v_rcp_f32_e32 v184, v184
	v_rcp_f32_e32 v185, v185
	v_rcp_f32_e32 v186, v186
	v_rcp_f32_e32 v187, v187
	v_rcp_f32_e32 v188, v188
	v_rcp_f32_e32 v189, v189
	v_rcp_f32_e32 v190, v190
	v_rcp_f32_e32 v191, v191
	v_rcp_f32_e32 v192, v192
	v_rcp_f32_e32 v193, v193
	v_mul_f32_e32 v178, v175, v178
	v_mul_f32_e32 v179, v175, v179
	v_mul_f32_e32 v180, v175, v180
	v_mul_f32_e32 v181, v175, v181
	v_mul_f32_e32 v182, v175, v182
	v_mul_f32_e32 v183, v175, v183
	v_mul_f32_e32 v184, v175, v184
	v_mul_f32_e32 v185, v175, v185
	v_exp_f32_e32 v104, v178
	v_exp_f32_e32 v105, v179
	v_exp_f32_e32 v106, v180
	v_exp_f32_e32 v107, v181
	v_exp_f32_e32 v108, v182
	v_exp_f32_e32 v109, v183
	v_exp_f32_e32 v110, v184
	v_exp_f32_e32 v111, v185
	s_nop 0
	v_fma_f32 v194, -v104, v104, 1.0
	v_fma_f32 v195, -v105, v105, 1.0
	v_fma_f32 v196, -v106, v106, 1.0
	v_fma_f32 v197, -v107, v107, 1.0
	v_fma_f32 v198, -v108, v108, 1.0
	v_fma_f32 v199, -v109, v109, 1.0
	v_fma_f32 v200, -v110, v110, 1.0
	v_fma_f32 v201, -v111, v111, 1.0
	v_max_f32_e32 v194, 0, v194
	v_max_f32_e32 v195, 0, v195
	v_max_f32_e32 v196, 0, v196
	v_max_f32_e32 v197, 0, v197
	v_max_f32_e32 v198, 0, v198
	v_max_f32_e32 v199, 0, v199
	v_max_f32_e32 v200, 0, v200
	v_max_f32_e32 v201, 0, v201
	v_sqrt_f32_e32 v194, v194
	v_sqrt_f32_e32 v195, v195
	v_sqrt_f32_e32 v196, v196
	v_sqrt_f32_e32 v197, v197
	v_sqrt_f32_e32 v198, v198
	v_sqrt_f32_e32 v199, v199
	v_sqrt_f32_e32 v200, v200
	v_sqrt_f32_e32 v201, v201
	s_waitcnt lgkmcnt(0)
	v_lshlrev_b32_e32 v152, 16, v152
	v_lshlrev_b32_e32 v153, 16, v153
	v_lshlrev_b32_e32 v154, 16, v154
	v_lshlrev_b32_e32 v155, 16, v155
	v_lshlrev_b32_e32 v156, 16, v156
	v_lshlrev_b32_e32 v157, 16, v157
	v_lshlrev_b32_e32 v158, 16, v158
	v_lshlrev_b32_e32 v159, 16, v159
	v_mul_f32_e32 v194, v194, v186
	v_mul_f32_e32 v195, v195, v187
	v_mul_f32_e32 v196, v196, v188
	v_mul_f32_e32 v197, v197, v189
	v_mul_f32_e32 v198, v198, v190
	v_mul_f32_e32 v199, v199, v191
	v_mul_f32_e32 v200, v200, v192
	v_mul_f32_e32 v201, v201, v193
	v_mul_f32_e32 v152, v194, v152
	v_mul_f32_e32 v153, v195, v153
	v_mul_f32_e32 v154, v196, v154
	v_mul_f32_e32 v155, v197, v155
	v_mul_f32_e32 v156, v198, v156
	v_mul_f32_e32 v157, v199, v157
	v_mul_f32_e32 v158, v200, v158
	v_mul_f32_e32 v159, v201, v159
	v_fma_f32 v145, v97, v144, v145
	v_fma_f32 v149, v101, v148, v149
	v_fma_f32 v153, v105, v152, v153
	v_fma_f32 v157, v109, v156, v157
	v_mul_f32_e32 v97, v97, v96
	v_mul_f32_e32 v101, v101, v100
	v_mul_f32_e32 v105, v105, v104
	v_mul_f32_e32 v109, v109, v108
	v_fma_f32 v146, v98, v145, v146
	v_fma_f32 v150, v102, v149, v150
	v_fma_f32 v154, v106, v153, v154
	v_fma_f32 v158, v110, v157, v158
	v_mul_f32_e32 v98, v98, v97
	v_mul_f32_e32 v102, v102, v101
	v_mul_f32_e32 v106, v106, v105
	v_mul_f32_e32 v110, v110, v109
	v_fma_f32 v147, v99, v146, v147
	v_fma_f32 v151, v103, v150, v151
	v_fma_f32 v155, v107, v154, v155
	v_fma_f32 v159, v111, v158, v159
	v_mul_f32_e32 v99, v99, v98
	v_mul_f32_e32 v103, v103, v102
	v_mul_f32_e32 v107, v107, v106
	v_mul_f32_e32 v111, v111, v110
	ds_bpermute_b32 v178, v204, v99
	ds_bpermute_b32 v182, v204, v147
	ds_bpermute_b32 v179, v204, v103
	ds_bpermute_b32 v183, v204, v151
	ds_bpermute_b32 v180, v204, v107
	ds_bpermute_b32 v184, v204, v155
	ds_bpermute_b32 v181, v204, v111
	ds_bpermute_b32 v185, v204, v159
	s_waitcnt lgkmcnt(0)
	v_fma_f32 v186, v182, v99, v147
	v_cndmask_b32_e64 v178, 1.0, v178, s[34:35]
	v_fma_f32 v187, v183, v103, v151
	v_cndmask_b32_e64 v179, 1.0, v179, s[34:35]
	v_fma_f32 v188, v184, v107, v155
	v_cndmask_b32_e64 v180, 1.0, v180, s[34:35]
	v_fma_f32 v189, v185, v111, v159
	v_cndmask_b32_e64 v181, 1.0, v181, s[34:35]
	v_cndmask_b32_e64 v223, v147, v186, s[34:35]
	v_mul_f32_e32 v219, v99, v178
	v_cndmask_b32_e64 v224, v151, v187, s[34:35]
	v_mul_f32_e32 v220, v103, v179
	v_cndmask_b32_e64 v225, v155, v188, s[34:35]
	v_mul_f32_e32 v221, v107, v180
	v_cndmask_b32_e64 v226, v159, v189, s[34:35]
	v_mul_f32_e32 v222, v111, v181
	ds_bpermute_b32 v178, v205, v219
	ds_bpermute_b32 v182, v205, v223
	ds_bpermute_b32 v179, v205, v220
	ds_bpermute_b32 v183, v205, v224
	ds_bpermute_b32 v180, v205, v221
	ds_bpermute_b32 v184, v205, v225
	ds_bpermute_b32 v181, v205, v222
	ds_bpermute_b32 v185, v205, v226
	s_waitcnt lgkmcnt(0)
	v_fma_f32 v186, v182, v219, v223
	v_cndmask_b32_e64 v178, 1.0, v178, s[36:37]
	v_fma_f32 v187, v183, v220, v224
	v_cndmask_b32_e64 v179, 1.0, v179, s[36:37]
	v_fma_f32 v188, v184, v221, v225
	v_cndmask_b32_e64 v180, 1.0, v180, s[36:37]
	v_fma_f32 v189, v185, v222, v226
	v_cndmask_b32_e64 v181, 1.0, v181, s[36:37]
	v_cndmask_b32_e64 v223, v223, v186, s[36:37]
	v_mul_f32_e32 v219, v219, v178
	v_cndmask_b32_e64 v224, v224, v187, s[36:37]
	v_mul_f32_e32 v220, v220, v179
	v_cndmask_b32_e64 v225, v225, v188, s[36:37]
	v_mul_f32_e32 v221, v221, v180
	v_cndmask_b32_e64 v226, v226, v189, s[36:37]
	v_mul_f32_e32 v222, v222, v181
	ds_bpermute_b32 v227, v204, v219
	ds_bpermute_b32 v231, v204, v223
	ds_bpermute_b32 v235, v206, v219
	ds_bpermute_b32 v239, v206, v223
	ds_bpermute_b32 v228, v204, v220
	ds_bpermute_b32 v232, v204, v224
	ds_bpermute_b32 v236, v206, v220
	ds_bpermute_b32 v244, v206, v224
	ds_bpermute_b32 v229, v204, v221
	ds_bpermute_b32 v233, v204, v225
	ds_bpermute_b32 v237, v206, v221
	ds_bpermute_b32 v245, v206, v225
	ds_bpermute_b32 v230, v204, v222
	ds_bpermute_b32 v234, v204, v226
	ds_bpermute_b32 v238, v206, v222
	ds_bpermute_b32 v246, v206, v226
	s_waitcnt lgkmcnt(0)
	v_cndmask_b32_e64 v227, 1.0, v227, s[34:35]
	v_cndmask_b32_e64 v231, 0, v231, s[34:35]
	v_cndmask_b32_e64 v228, 1.0, v228, s[34:35]
	v_cndmask_b32_e64 v232, 0, v232, s[34:35]
	v_cndmask_b32_e64 v229, 1.0, v229, s[34:35]
	v_cndmask_b32_e64 v233, 0, v233, s[34:35]
	v_cndmask_b32_e64 v230, 1.0, v230, s[34:35]
	v_cndmask_b32_e64 v234, 0, v234, s[34:35]
	v_mov_b32_e32 v190, v235
	v_mov_b32_e32 v194, v239
	v_mov_b32_e32 v198, v190
	v_mov_b32_e32 v201, v194
	v_fma_f32 v194, v194, v236, v244
	v_mul_f32_e32 v190, v190, v236
	v_mov_b32_e32 v199, v190
	v_mov_b32_e32 v177, v194
	v_fma_f32 v194, v194, v237, v245
	v_mul_f32_e32 v190, v190, v237
	v_mov_b32_e32 v200, v190
	v_mov_b32_e32 v203, v194
	v_fma_f32 v194, v194, v238, v246
	v_mul_f32_e32 v190, v190, v238
	v_mov_b32_e32 v191, v194
	ds_write_b64 v207, v[190:191]
	s_waitcnt lgkmcnt(0)
	s_barrier
	ds_read_b64 v[178:179], v208
	ds_read_b64 v[180:181], v208 offset:512
	s_waitcnt lgkmcnt(0)
	v_fma_f32 v182, v176, v178, v179
	v_cndmask_b32_e64 v183, v176, v182, s[38:39]
	v_fma_f32 v176, v182, v180, v181
	s_add_i32 s13, s13, 1
	s_waitcnt vmcnt(0)
	s_barrier
	s_cmp_gt_u32 s13, 15
	s_cbranch_scc1 .Lmylru_nopf_2
	s_add_i32 s58, s13, 2
	s_cmp_lt_u32 s58, 2
	s_lshl_b32 s50, s58, 7
	s_lshl_b32 s51, s9, 8
	s_add_i32 s51, s51, 0x8000
	s_add_i32 s51, s51, s50
	s_lshl_b32 s59, s9, 11
	s_add_i32 s59, s59, s50
	s_addk_i32 s59, 0xff00
	s_cmp_lt_u32 s58, 2
	s_cselect_b32 s59, s51, s59
	s_lshl_b32 s52, s59, 11
	s_add_u32 s46, s16, s52
	s_addc_u32 s47, s17, 0
	s_lshl_b32 s52, s6, 10
	s_add_i32 s52, s52, 0x24800
	s_mov_b32 m0, s52
	s_nop 0
	global_load_lds_dwordx4 v169, s[46:47]
.Lmylru_nopf_2:
	s_cmp_eq_u32 s13, 17
	s_cbranch_scc1 .Lmylru_nodma_2
	s_add_i32 s58, s13, 1
	s_cmp_lt_u32 s58, 2
	s_lshl_b32 s50, s58, 7
	s_lshl_b32 s51, s9, 8
	s_add_i32 s51, s51, 0x8000
	s_add_i32 s51, s51, s50
	s_lshl_b32 s59, s9, 11
	s_add_i32 s59, s59, s50
	s_addk_i32 s59, 0xff00
	s_cmp_lt_u32 s58, 2
	s_cselect_b32 s59, s51, s59
	s_lshl_b32 s52, s59, 11
	s_add_u32 s46, s16, s52
	s_addc_u32 s47, s17, 0
	s_lshl_b32 s52, s6, 13
	s_mov_b32 m0, s52
	s_add_i32 s52, s52, 0x400
	global_load_lds_dwordx4 v211, s[46:47]
	s_mov_b32 m0, s52
	s_add_i32 s52, s52, 0x400
	global_load_lds_dwordx4 v212, s[46:47]
	s_mov_b32 m0, s52
	s_add_i32 s52, s52, 0x400
	global_load_lds_dwordx4 v213, s[46:47]
	s_mov_b32 m0, s52
	s_add_i32 s52, s52, 0x400
	global_load_lds_dwordx4 v214, s[46:47]
	s_mov_b32 m0, s52
	s_add_i32 s52, s52, 0x400
	global_load_lds_dwordx4 v215, s[46:47]
	s_mov_b32 m0, s52
	s_add_i32 s52, s52, 0x400
	global_load_lds_dwordx4 v216, s[46:47]
	s_mov_b32 m0, s52
	s_add_i32 s52, s52, 0x400
	global_load_lds_dwordx4 v217, s[46:47]
	s_mov_b32 m0, s52
	s_nop 0
	global_load_lds_dwordx4 v218, s[46:47]

.Lmylru_t1_3:
	s_barrier
	s_add_i32 s54, s13, -2
	s_lshl_b32 s55, s54, 14
	s_lshl_b32 s56, s6, 11
	s_add_i32 s55, s55, s56
	s_add_u32 s44, s22, s55
	s_addc_u32 s45, s23, 0
	s_cmp_gt_u32 s13, 15
	s_cbranch_scc1 .Lmylru_nopf_3
	s_add_i32 s58, s13, 2
	s_cmp_lt_u32 s58, 2
	s_lshl_b32 s50, s58, 7
	s_lshl_b32 s51, s9, 8
	s_add_i32 s51, s51, 0x8000
	s_add_i32 s51, s51, s50
	s_lshl_b32 s59, s9, 11
	s_add_i32 s59, s59, s50
	s_addk_i32 s59, 0xff00
	s_cmp_lt_u32 s58, 2
	s_cselect_b32 s59, s51, s59
	s_lshl_b32 s52, s59, 11
	s_add_u32 s46, s16, s52
	s_addc_u32 s47, s17, 0
	s_lshl_b32 s52, s6, 10
	s_add_i32 s52, s52, 0x24800
	s_mov_b32 m0, s52
	s_nop 0
	global_load_lds_dwordx4 v169, s[46:47]

.Lmylru_nodma_4:
	v_or_b32_e32 v163, 0x10000, v162
	ds_read_b128 v[96:99], v163
	ds_read_b128 v[100:103], v163 offset:8192
	ds_read_b128 v[104:107], v163 offset:16384
	ds_read_b128 v[108:111], v163 offset:24576
	v_xor_b32_e32 v164, 0x40, v163
	ds_read_b128 v[112:115], v164
	ds_read_b128 v[116:119], v164 offset:8192
	ds_read_b128 v[120:123], v164 offset:16384
	ds_read_b128 v[124:127], v164 offset:24576
	s_waitcnt lgkmcnt(7)
	v_mfma_f32_16x16x32_bf16 v[64:67], v[96:99], v[0:3], 0
	v_mfma_f32_16x16x32_bf16 v[68:71], v[96:99], v[32:35], 0
	v_xor_b32_e32 v164, 0x80, v163
	ds_read_b128 v[96:99], v164
	s_waitcnt lgkmcnt(7)
	v_mfma_f32_16x16x32_bf16 v[72:75], v[100:103], v[0:3], 0
	v_mfma_f32_16x16x32_bf16 v[76:79], v[100:103], v[32:35], 0
	ds_read_b128 v[100:103], v164 offset:8192
	s_waitcnt lgkmcnt(7)
	v_mfma_f32_16x16x32_bf16 v[80:83], v[104:107], v[0:3], 0
	v_mfma_f32_16x16x32_bf16 v[84:87], v[104:107], v[32:35], 0
	ds_read_b128 v[104:107], v164 offset:16384
	s_waitcnt lgkmcnt(7)
	v_mfma_f32_16x16x32_bf16 v[88:91], v[108:111], v[0:3], 0
	v_mfma_f32_16x16x32_bf16 v[92:95], v[108:111], v[32:35], 0
	ds_read_b128 v[108:111], v164 offset:24576
	s_waitcnt lgkmcnt(7)
	v_mfma_f32_16x16x32_bf16 v[64:67], v[112:115], v[4:7], v[64:67]
	v_mfma_f32_16x16x32_bf16 v[68:71], v[112:115], v[36:39], v[68:71]
	v_xor_b32_e32 v164, 0xc0, v163
	ds_read_b128 v[112:115], v164
	s_waitcnt lgkmcnt(7)
	v_mfma_f32_16x16x32_bf16 v[72:75], v[116:119], v[4:7], v[72:75]
	v_mfma_f32_16x16x32_bf16 v[76:79], v[116:119], v[36:39], v[76:79]
	ds_read_b128 v[116:119], v164 offset:8192
	s_waitcnt lgkmcnt(7)
	v_mfma_f32_16x16x32_bf16 v[80:83], v[120:123], v[4:7], v[80:83]
	v_mfma_f32_16x16x32_bf16 v[84:87], v[120:123], v[36:39], v[84:87]
	ds_read_b128 v[120:123], v164 offset:16384
	s_waitcnt lgkmcnt(7)
	v_mfma_f32_16x16x32_bf16 v[88:91], v[124:127], v[4:7], v[88:91]
	v_mfma_f32_16x16x32_bf16 v[92:95], v[124:127], v[36:39], v[92:95]
	ds_read_b128 v[124:127], v164 offset:24576
	s_waitcnt lgkmcnt(7)
	v_mfma_f32_16x16x32_bf16 v[64:67], v[96:99], v[8:11], v[64:67]
	v_mfma_f32_16x16x32_bf16 v[68:71], v[96:99], v[40:43], v[68:71]
	v_xor_b32_e32 v164, 0x100, v163
	ds_read_b128 v[96:99], v164
	s_waitcnt lgkmcnt(7)
	v_mfma_f32_16x16x32_bf16 v[72:75], v[100:103], v[8:11], v[72:75]
	v_mfma_f32_16x16x32_bf16 v[76:79], v[100:103], v[40:43], v[76:79]
	ds_read_b128 v[100:103], v164 offset:8192
	s_waitcnt lgkmcnt(7)
	v_mfma_f32_16x16x32_bf16 v[80:83], v[104:107], v[8:11], v[80:83]
	v_mfma_f32_16x16x32_bf16 v[84:87], v[104:107], v[40:43], v[84:87]
	ds_read_b128 v[104:107], v164 offset:16384
	s_waitcnt lgkmcnt(7)
	v_mfma_f32_16x16x32_bf16 v[88:91], v[108:111], v[8:11], v[88:91]
	v_mfma_f32_16x16x32_bf16 v[92:95], v[108:111], v[40:43], v[92:95]
	ds_read_b128 v[108:111], v164 offset:24576
	s_waitcnt lgkmcnt(7)
	v_mfma_f32_16x16x32_bf16 v[64:67], v[112:115], v[12:15], v[64:67]
	v_mfma_f32_16x16x32_bf16 v[68:71], v[112:115], v[44:47], v[68:71]
	v_xor_b32_e32 v164, 0x140, v163
	ds_read_b128 v[112:115], v164
	s_waitcnt lgkmcnt(7)
	v_mfma_f32_16x16x32_bf16 v[72:75], v[116:119], v[12:15], v[72:75]
	v_mfma_f32_16x16x32_bf16 v[76:79], v[116:119], v[44:47], v[76:79]
	ds_read_b128 v[116:119], v164 offset:8192
	s_waitcnt lgkmcnt(7)
	v_mfma_f32_16x16x32_bf16 v[80:83], v[120:123], v[12:15], v[80:83]
	v_mfma_f32_16x16x32_bf16 v[84:87], v[120:123], v[44:47], v[84:87]
	ds_read_b128 v[120:123], v164 offset:16384
	s_waitcnt lgkmcnt(7)
	v_mfma_f32_16x16x32_bf16 v[88:91], v[124:127], v[12:15], v[88:91]
	v_mfma_f32_16x16x32_bf16 v[92:95], v[124:127], v[44:47], v[92:95]
	ds_read_b128 v[124:127], v164 offset:24576
	s_waitcnt lgkmcnt(7)
	v_mfma_f32_16x16x32_bf16 v[64:67], v[96:99], v[16:19], v[64:67]
	v_mfma_f32_16x16x32_bf16 v[68:71], v[96:99], v[48:51], v[68:71]
	v_xor_b32_e32 v164, 0x180, v163
	ds_read_b128 v[96:99], v164
	s_waitcnt lgkmcnt(7)
	v_mfma_f32_16x16x32_bf16 v[72:75], v[100:103], v[16:19], v[72:75]
	v_mfma_f32_16x16x32_bf16 v[76:79], v[100:103], v[48:51], v[76:79]
	ds_read_b128 v[100:103], v164 offset:8192
	s_waitcnt lgkmcnt(7)
	v_mfma_f32_16x16x32_bf16 v[80:83], v[104:107], v[16:19], v[80:83]
	v_mfma_f32_16x16x32_bf16 v[84:87], v[104:107], v[48:51], v[84:87]
	ds_read_b128 v[104:107], v164 offset:16384
	s_waitcnt lgkmcnt(7)
	v_mfma_f32_16x16x32_bf16 v[88:91], v[108:111], v[16:19], v[88:91]
	v_mfma_f32_16x16x32_bf16 v[92:95], v[108:111], v[48:51], v[92:95]
	ds_read_b128 v[108:111], v164 offset:24576
	s_waitcnt lgkmcnt(7)
	v_mfma_f32_16x16x32_bf16 v[64:67], v[112:115], v[20:23], v[64:67]
	v_mfma_f32_16x16x32_bf16 v[68:71], v[112:115], v[52:55], v[68:71]
	v_xor_b32_e32 v164, 0x1c0, v163
	ds_read_b128 v[112:115], v164
	s_waitcnt lgkmcnt(7)
	v_mfma_f32_16x16x32_bf16 v[72:75], v[116:119], v[20:23], v[72:75]
	v_mfma_f32_16x16x32_bf16 v[76:79], v[116:119], v[52:55], v[76:79]
	ds_read_b128 v[116:119], v164 offset:8192
	s_waitcnt lgkmcnt(7)
	v_mfma_f32_16x16x32_bf16 v[80:83], v[120:123], v[20:23], v[80:83]
	v_mfma_f32_16x16x32_bf16 v[84:87], v[120:123], v[52:55], v[84:87]
	ds_read_b128 v[120:123], v164 offset:16384
	s_waitcnt lgkmcnt(7)
	v_mfma_f32_16x16x32_bf16 v[88:91], v[124:127], v[20:23], v[88:91]
	v_mfma_f32_16x16x32_bf16 v[92:95], v[124:127], v[52:55], v[92:95]
	ds_read_b128 v[124:127], v164 offset:24576
	s_waitcnt lgkmcnt(7)
	v_mfma_f32_16x16x32_bf16 v[64:67], v[96:99], v[24:27], v[64:67]
	v_mfma_f32_16x16x32_bf16 v[68:71], v[96:99], v[56:59], v[68:71]
	s_waitcnt lgkmcnt(6)
	v_mfma_f32_16x16x32_bf16 v[72:75], v[100:103], v[24:27], v[72:75]
	v_mfma_f32_16x16x32_bf16 v[76:79], v[100:103], v[56:59], v[76:79]
	s_waitcnt lgkmcnt(5)
	v_mfma_f32_16x16x32_bf16 v[80:83], v[104:107], v[24:27], v[80:83]
	v_mfma_f32_16x16x32_bf16 v[84:87], v[104:107], v[56:59], v[84:87]
	s_waitcnt lgkmcnt(4)
	v_mfma_f32_16x16x32_bf16 v[88:91], v[108:111], v[24:27], v[88:91]
	v_mfma_f32_16x16x32_bf16 v[92:95], v[108:111], v[56:59], v[92:95]
	s_waitcnt lgkmcnt(3)
	v_mfma_f32_16x16x32_bf16 v[64:67], v[112:115], v[28:31], v[64:67]
	v_mfma_f32_16x16x32_bf16 v[68:71], v[112:115], v[60:63], v[68:71]
	s_waitcnt lgkmcnt(2)
	v_mfma_f32_16x16x32_bf16 v[72:75], v[116:119], v[28:31], v[72:75]
	v_mfma_f32_16x16x32_bf16 v[76:79], v[116:119], v[60:63], v[76:79]
	s_waitcnt lgkmcnt(1)
	v_mfma_f32_16x16x32_bf16 v[80:83], v[120:123], v[28:31], v[80:83]
	v_mfma_f32_16x16x32_bf16 v[84:87], v[120:123], v[60:63], v[84:87]
	s_waitcnt lgkmcnt(0)
	v_mfma_f32_16x16x32_bf16 v[88:91], v[124:127], v[28:31], v[88:91]
	v_mfma_f32_16x16x32_bf16 v[92:95], v[124:127], v[60:63], v[92:95]
	v_or_b32_e32 v198, 0x10000, v165
	v_or_b32_e32 v199, 0x10000, v166
	v_or_b32_e32 v200, 0x10000, v167
	v_or_b32_e32 v201, 0x10000, v168
	ds_read_u16 v144, v198
	ds_read_u16 v145, v199
	ds_read_u16 v146, v200
	ds_read_u16 v147, v201
	ds_read_u16 v148, v198 offset:8192
	ds_read_u16 v149, v199 offset:8192
	ds_read_u16 v150, v200 offset:8192
	ds_read_u16 v151, v201 offset:8192
	ds_read_u16 v152, v198 offset:16384
	ds_read_u16 v153, v199 offset:16384
	ds_read_u16 v154, v200 offset:16384
	ds_read_u16 v155, v201 offset:16384
	ds_read_u16 v156, v198 offset:24576
	ds_read_u16 v157, v199 offset:24576
	ds_read_u16 v158, v200 offset:24576
	ds_read_u16 v159, v201 offset:24576
	s_nop 7
	v_fma_f32 v178, v64, s53, v173
	v_fma_f32 v179, v65, s53, v173
	v_fma_f32 v180, v66, s53, v173
	v_fma_f32 v181, v67, s53, v173
	v_fma_f32 v182, v72, s53, v173
	v_fma_f32 v183, v73, s53, v173
	v_fma_f32 v184, v74, s53, v173
	v_fma_f32 v185, v75, s53, v173
	v_fma_f32 v186, v68, s53, v174
	v_fma_f32 v187, v69, s53, v174
	v_fma_f32 v188, v70, s53, v174
	v_fma_f32 v189, v71, s53, v174
	v_fma_f32 v190, v76, s53, v174
	v_fma_f32 v191, v77, s53, v174
	v_fma_f32 v192, v78, s53, v174
	v_fma_f32 v193, v79, s53, v174
	v_exp_f32_e32 v178, v178
	v_exp_f32_e32 v179, v179
	v_exp_f32_e32 v180, v180
	v_exp_f32_e32 v181, v181
	v_exp_f32_e32 v182, v182
	v_exp_f32_e32 v183, v183
	v_exp_f32_e32 v184, v184
	v_exp_f32_e32 v185, v185
	v_exp_f32_e32 v186, v186
	v_exp_f32_e32 v187, v187
	v_exp_f32_e32 v188, v188
	v_exp_f32_e32 v189, v189
	v_exp_f32_e32 v190, v190
	v_exp_f32_e32 v191, v191
	v_exp_f32_e32 v192, v192
	v_exp_f32_e32 v193, v193
	v_add_f32_e32 v178, 1.0, v178
	v_add_f32_e32 v179, 1.0, v179
	v_add_f32_e32 v180, 1.0, v180
	v_add_f32_e32 v181, 1.0, v181
	v_add_f32_e32 v182, 1.0, v182
	v_add_f32_e32 v183, 1.0, v183
	v_add_f32_e32 v184, 1.0, v184
	v_add_f32_e32 v185, 1.0, v185
	v_add_f32_e32 v186, 1.0, v186
	v_add_f32_e32 v187, 1.0, v187
	v_add_f32_e32 v188, 1.0, v188
	v_add_f32_e32 v189, 1.0, v189
	v_add_f32_e32 v190, 1.0, v190
	v_add_f32_e32 v191, 1.0, v191
	v_add_f32_e32 v192, 1.0, v192
	v_add_f32_e32 v193, 1.0, v193
	v_rcp_f32_e32 v178, v178
	v_rcp_f32_e32 v179, v179
	v_rcp_f32_e32 v180, v180
	v_rcp_f32_e32 v181, v181
	v_rcp_f32_e32 v182, v182
	v_rcp_f32_e32 v183, v183
	v_rcp_f32_e32 v184, v184
	v_rcp_f32_e32 v185, v185
	v_rcp_f32_e32 v186, v186
	v_rcp_f32_e32 v187, v187
	v_rcp_f32_e32 v188, v188
	v_rcp_f32_e32 v189, v189
	v_rcp_f32_e32 v190, v190
	v_rcp_f32_e32 v191, v191
	v_rcp_f32_e32 v192, v192
	v_rcp_f32_e32 v193, v193
	v_mul_f32_e32 v178, v175, v178
	v_mul_f32_e32 v179, v175, v179
	v_mul_f32_e32 v180, v175, v180
	v_mul_f32_e32 v181, v175, v181
	v_mul_f32_e32 v182, v175, v182
	v_mul_f32_e32 v183, v175, v183
	v_mul_f32_e32 v184, v175, v184
	v_mul_f32_e32 v185, v175, v185
	v_exp_f32_e32 v96, v178
	v_exp_f32_e32 v97, v179
	v_exp_f32_e32 v98, v180
	v_exp_f32_e32 v99, v181
	v_exp_f32_e32 v100, v182
	v_exp_f32_e32 v101, v183
	v_exp_f32_e32 v102, v184
	v_exp_f32_e32 v103, v185
	s_nop 0
	v_fma_f32 v194, -v96, v96, 1.0
	v_fma_f32 v195, -v97, v97, 1.0
	v_fma_f32 v196, -v98, v98, 1.0
	v_fma_f32 v197, -v99, v99, 1.0
	v_fma_f32 v198, -v100, v100, 1.0
	v_fma_f32 v199, -v101, v101, 1.0
	v_fma_f32 v200, -v102, v102, 1.0
	v_fma_f32 v201, -v103, v103, 1.0
	v_max_f32_e32 v194, 0, v194
	v_max_f32_e32 v195, 0, v195
	v_max_f32_e32 v196, 0, v196
	v_max_f32_e32 v197, 0, v197
	v_max_f32_e32 v198, 0, v198
	v_max_f32_e32 v199, 0, v199
	v_max_f32_e32 v200, 0, v200
	v_max_f32_e32 v201, 0, v201
	v_sqrt_f32_e32 v194, v194
	v_sqrt_f32_e32 v195, v195
	v_sqrt_f32_e32 v196, v196
	v_sqrt_f32_e32 v197, v197
	v_sqrt_f32_e32 v198, v198
	v_sqrt_f32_e32 v199, v199
	v_sqrt_f32_e32 v200, v200
	v_sqrt_f32_e32 v201, v201
	s_waitcnt lgkmcnt(8)
	v_lshlrev_b32_e32 v144, 16, v144
	v_lshlrev_b32_e32 v145, 16, v145
	v_lshlrev_b32_e32 v146, 16, v146
	v_lshlrev_b32_e32 v147, 16, v147
	v_lshlrev_b32_e32 v148, 16, v148
	v_lshlrev_b32_e32 v149, 16, v149
	v_lshlrev_b32_e32 v150, 16, v150
	v_lshlrev_b32_e32 v151, 16, v151
	v_mul_f32_e32 v194, v194, v186
	v_mul_f32_e32 v195, v195, v187
	v_mul_f32_e32 v196, v196, v188
	v_mul_f32_e32 v197, v197, v189
	v_mul_f32_e32 v198, v198, v190
	v_mul_f32_e32 v199, v199, v191
	v_mul_f32_e32 v200, v200, v192
	v_mul_f32_e32 v201, v201, v193
	v_mul_f32_e32 v144, v194, v144
	v_mul_f32_e32 v145, v195, v145
	v_mul_f32_e32 v146, v196, v146
	v_mul_f32_e32 v147, v197, v147
	v_mul_f32_e32 v148, v198, v148
	v_mul_f32_e32 v149, v199, v149
	v_mul_f32_e32 v150, v200, v150
	v_mul_f32_e32 v151, v201, v151
	v_fma_f32 v178, v80, s53, v173
	v_fma_f32 v179, v81, s53, v173
	v_fma_f32 v180, v82, s53, v173
	v_fma_f32 v181, v83, s53, v173
	v_fma_f32 v182, v88, s53, v173
	v_fma_f32 v183, v89, s53, v173
	v_fma_f32 v184, v90, s53, v173
	v_fma_f32 v185, v91, s53, v173
	v_fma_f32 v186, v84, s53, v174
	v_fma_f32 v187, v85, s53, v174
	v_fma_f32 v188, v86, s53, v174
	v_fma_f32 v189, v87, s53, v174
	v_fma_f32 v190, v92, s53, v174
	v_fma_f32 v191, v93, s53, v174
	v_fma_f32 v192, v94, s53, v174
	v_fma_f32 v193, v95, s53, v174
	v_exp_f32_e32 v178, v178
	v_exp_f32_e32 v179, v179
	v_exp_f32_e32 v180, v180
	v_exp_f32_e32 v181, v181
	v_exp_f32_e32 v182, v182
	v_exp_f32_e32 v183, v183
	v_exp_f32_e32 v184, v184
	v_exp_f32_e32 v185, v185
	v_exp_f32_e32 v186, v186
	v_exp_f32_e32 v187, v187
	v_exp_f32_e32 v188, v188
	v_exp_f32_e32 v189, v189
	v_exp_f32_e32 v190, v190
	v_exp_f32_e32 v191, v191
	v_exp_f32_e32 v192, v192
	v_exp_f32_e32 v193, v193
	v_add_f32_e32 v178, 1.0, v178
	v_add_f32_e32 v179, 1.0, v179
	v_add_f32_e32 v180, 1.0, v180
	v_add_f32_e32 v181, 1.0, v181
	v_add_f32_e32 v182, 1.0, v182
	v_add_f32_e32 v183, 1.0, v183
	v_add_f32_e32 v184, 1.0, v184
	v_add_f32_e32 v185, 1.0, v185
	v_add_f32_e32 v186, 1.0, v186
	v_add_f32_e32 v187, 1.0, v187
	v_add_f32_e32 v188, 1.0, v188
	v_add_f32_e32 v189, 1.0, v189
	v_add_f32_e32 v190, 1.0, v190
	v_add_f32_e32 v191, 1.0, v191
	v_add_f32_e32 v192, 1.0, v192
	v_add_f32_e32 v193, 1.0, v193
	v_rcp_f32_e32 v178, v178
	v_rcp_f32_e32 v179, v179
	v_rcp_f32_e32 v180, v180
	v_rcp_f32_e32 v181, v181
	v_rcp_f32_e32 v182, v182
	v_rcp_f32_e32 v183, v183
	v_rcp_f32_e32 v184, v184
	v_rcp_f32_e32 v185, v185
	v_rcp_f32_e32 v186, v186
	v_rcp_f32_e32 v187, v187
	v_rcp_f32_e32 v188, v188
	v_rcp_f32_e32 v189, v189
	v_rcp_f32_e32 v190, v190
	v_rcp_f32_e32 v191, v191
	v_rcp_f32_e32 v192, v192
	v_rcp_f32_e32 v193, v193
	v_mul_f32_e32 v178, v175, v178
	v_mul_f32_e32 v179, v175, v179
	v_mul_f32_e32 v180, v175, v180
	v_mul_f32_e32 v181, v175, v181
	v_mul_f32_e32 v182, v175, v182
	v_mul_f32_e32 v183, v175, v183
	v_mul_f32_e32 v184, v175, v184
	v_mul_f32_e32 v185, v175, v185
	v_exp_f32_e32 v104, v178
	v_exp_f32_e32 v105, v179
	v_exp_f32_e32 v106, v180
	v_exp_f32_e32 v107, v181
	v_exp_f32_e32 v108, v182
	v_exp_f32_e32 v109, v183
	v_exp_f32_e32 v110, v184
	v_exp_f32_e32 v111, v185
	s_nop 0
	v_fma_f32 v194, -v104, v104, 1.0
	v_fma_f32 v195, -v105, v105, 1.0
	v_fma_f32 v196, -v106, v106, 1.0
	v_fma_f32 v197, -v107, v107, 1.0
	v_fma_f32 v198, -v108, v108, 1.0
	v_fma_f32 v199, -v109, v109, 1.0
	v_fma_f32 v200, -v110, v110, 1.0
	v_fma_f32 v201, -v111, v111, 1.0
	v_max_f32_e32 v194, 0, v194
	v_max_f32_e32 v195, 0, v195
	v_max_f32_e32 v196, 0, v196
	v_max_f32_e32 v197, 0, v197
	v_max_f32_e32 v198, 0, v198
	v_max_f32_e32 v199, 0, v199
	v_max_f32_e32 v200, 0, v200
	v_max_f32_e32 v201, 0, v201
	v_sqrt_f32_e32 v194, v194
	v_sqrt_f32_e32 v195, v195
	v_sqrt_f32_e32 v196, v196
	v_sqrt_f32_e32 v197, v197
	v_sqrt_f32_e32 v198, v198
	v_sqrt_f32_e32 v199, v199
	v_sqrt_f32_e32 v200, v200
	v_sqrt_f32_e32 v201, v201
	s_waitcnt lgkmcnt(0)
	v_lshlrev_b32_e32 v152, 16, v152
	v_lshlrev_b32_e32 v153, 16, v153
	v_lshlrev_b32_e32 v154, 16, v154
	v_lshlrev_b32_e32 v155, 16, v155
	v_lshlrev_b32_e32 v156, 16, v156
	v_lshlrev_b32_e32 v157, 16, v157
	v_lshlrev_b32_e32 v158, 16, v158
	v_lshlrev_b32_e32 v159, 16, v159
	v_mul_f32_e32 v194, v194, v186
	v_mul_f32_e32 v195, v195, v187
	v_mul_f32_e32 v196, v196, v188
	v_mul_f32_e32 v197, v197, v189
	v_mul_f32_e32 v198, v198, v190
	v_mul_f32_e32 v199, v199, v191
	v_mul_f32_e32 v200, v200, v192
	v_mul_f32_e32 v201, v201, v193
	v_mul_f32_e32 v152, v194, v152
	v_mul_f32_e32 v153, v195, v153
	v_mul_f32_e32 v154, v196, v154
	v_mul_f32_e32 v155, v197, v155
	v_mul_f32_e32 v156, v198, v156
	v_mul_f32_e32 v157, v199, v157
	v_mul_f32_e32 v158, v200, v158
	v_mul_f32_e32 v159, v201, v159
	v_fma_f32 v145, v97, v144, v145
	v_fma_f32 v149, v101, v148, v149
	v_fma_f32 v153, v105, v152, v153
	v_fma_f32 v157, v109, v156, v157
	v_mul_f32_e32 v97, v97, v96
	v_mul_f32_e32 v101, v101, v100
	v_mul_f32_e32 v105, v105, v104
	v_mul_f32_e32 v109, v109, v108
	v_fma_f32 v146, v98, v145, v146
	v_fma_f32 v150, v102, v149, v150
	v_fma_f32 v154, v106, v153, v154
	v_fma_f32 v158, v110, v157, v158
	v_mul_f32_e32 v98, v98, v97
	v_mul_f32_e32 v102, v102, v101
	v_mul_f32_e32 v106, v106, v105
	v_mul_f32_e32 v110, v110, v109
	v_fma_f32 v147, v99, v146, v147
	v_fma_f32 v151, v103, v150, v151
	v_fma_f32 v155, v107, v154, v155
	v_fma_f32 v159, v111, v158, v159
	v_mul_f32_e32 v99, v99, v98
	v_mul_f32_e32 v103, v103, v102
	v_mul_f32_e32 v107, v107, v106
	v_mul_f32_e32 v111, v111, v110
	ds_bpermute_b32 v178, v204, v99
	ds_bpermute_b32 v182, v204, v147
	ds_bpermute_b32 v179, v204, v103
	ds_bpermute_b32 v183, v204, v151
	ds_bpermute_b32 v180, v204, v107
	ds_bpermute_b32 v184, v204, v155
	ds_bpermute_b32 v181, v204, v111
	ds_bpermute_b32 v185, v204, v159
	s_waitcnt lgkmcnt(0)
	v_fma_f32 v186, v182, v99, v147
	v_cndmask_b32_e64 v178, 1.0, v178, s[34:35]
	v_fma_f32 v187, v183, v103, v151
	v_cndmask_b32_e64 v179, 1.0, v179, s[34:35]
	v_fma_f32 v188, v184, v107, v155
	v_cndmask_b32_e64 v180, 1.0, v180, s[34:35]
	v_fma_f32 v189, v185, v111, v159
	v_cndmask_b32_e64 v181, 1.0, v181, s[34:35]
	v_cndmask_b32_e64 v223, v147, v186, s[34:35]
	v_mul_f32_e32 v219, v99, v178
	v_cndmask_b32_e64 v224, v151, v187, s[34:35]
	v_mul_f32_e32 v220, v103, v179
	v_cndmask_b32_e64 v225, v155, v188, s[34:35]
	v_mul_f32_e32 v221, v107, v180
	v_cndmask_b32_e64 v226, v159, v189, s[34:35]
	v_mul_f32_e32 v222, v111, v181
	ds_bpermute_b32 v178, v205, v219
	ds_bpermute_b32 v182, v205, v223
	ds_bpermute_b32 v179, v205, v220
	ds_bpermute_b32 v183, v205, v224
	ds_bpermute_b32 v180, v205, v221
	ds_bpermute_b32 v184, v205, v225
	ds_bpermute_b32 v181, v205, v222
	ds_bpermute_b32 v185, v205, v226
	s_waitcnt lgkmcnt(0)
	v_fma_f32 v186, v182, v219, v223
	v_cndmask_b32_e64 v178, 1.0, v178, s[36:37]
	v_fma_f32 v187, v183, v220, v224
	v_cndmask_b32_e64 v179, 1.0, v179, s[36:37]
	v_fma_f32 v188, v184, v221, v225
	v_cndmask_b32_e64 v180, 1.0, v180, s[36:37]
	v_fma_f32 v189, v185, v222, v226
	v_cndmask_b32_e64 v181, 1.0, v181, s[36:37]
	v_cndmask_b32_e64 v223, v223, v186, s[36:37]
	v_mul_f32_e32 v219, v219, v178
	v_cndmask_b32_e64 v224, v224, v187, s[36:37]
	v_mul_f32_e32 v220, v220, v179
	v_cndmask_b32_e64 v225, v225, v188, s[36:37]
	v_mul_f32_e32 v221, v221, v180
	v_cndmask_b32_e64 v226, v226, v189, s[36:37]
	v_mul_f32_e32 v222, v222, v181
	ds_bpermute_b32 v227, v204, v219
	ds_bpermute_b32 v231, v204, v223
	ds_bpermute_b32 v235, v206, v219
	ds_bpermute_b32 v239, v206, v223
	ds_bpermute_b32 v228, v204, v220
	ds_bpermute_b32 v232, v204, v224
	ds_bpermute_b32 v236, v206, v220
	ds_bpermute_b32 v244, v206, v224
	ds_bpermute_b32 v229, v204, v221
	ds_bpermute_b32 v233, v204, v225
	ds_bpermute_b32 v237, v206, v221
	ds_bpermute_b32 v245, v206, v225
	ds_bpermute_b32 v230, v204, v222
	ds_bpermute_b32 v234, v204, v226
	ds_bpermute_b32 v238, v206, v222
	ds_bpermute_b32 v246, v206, v226
	s_waitcnt lgkmcnt(0)
	v_cndmask_b32_e64 v227, 1.0, v227, s[34:35]
	v_cndmask_b32_e64 v231, 0, v231, s[34:35]
	v_cndmask_b32_e64 v228, 1.0, v228, s[34:35]
	v_cndmask_b32_e64 v232, 0, v232, s[34:35]
	v_cndmask_b32_e64 v229, 1.0, v229, s[34:35]
	v_cndmask_b32_e64 v233, 0, v233, s[34:35]
	v_cndmask_b32_e64 v230, 1.0, v230, s[34:35]
	v_cndmask_b32_e64 v234, 0, v234, s[34:35]
	v_mov_b32_e32 v190, v235
	v_mov_b32_e32 v194, v239
	v_mov_b32_e32 v198, v190
	v_mov_b32_e32 v201, v194
	v_fma_f32 v194, v194, v236, v244
	v_mul_f32_e32 v190, v190, v236
	v_mov_b32_e32 v199, v190
	v_mov_b32_e32 v177, v194
	v_fma_f32 v194, v194, v237, v245
	v_mul_f32_e32 v190, v190, v237
	v_mov_b32_e32 v200, v190
	v_mov_b32_e32 v203, v194
	v_fma_f32 v194, v194, v238, v246
	v_mul_f32_e32 v190, v190, v238
	v_mov_b32_e32 v191, v194
	ds_write_b64 v207, v[190:191] offset:1024
	s_waitcnt lgkmcnt(0)
	s_barrier
	ds_read_b64 v[178:179], v208 offset:1024
	ds_read_b64 v[180:181], v208 offset:1536
	s_waitcnt lgkmcnt(0)
	v_fma_f32 v182, v176, v178, v179
	v_cndmask_b32_e64 v183, v176, v182, s[38:39]
	v_fma_f32 v176, v182, v180, v181
	v_mov_b32_e32 v184, v183
	v_fma_f32 v185, v183, v198, v201
	v_fma_f32 v186, v183, v199, v177
	v_fma_f32 v187, v183, v200, v203
	v_fma_f32 v184, v184, v227, v231
	v_fma_f32 v185, v185, v228, v232
	v_fma_f32 v186, v186, v229, v233
	v_fma_f32 v187, v187, v230, v234
	v_fma_f32 v144, v184, v96, v144
	v_fma_f32 v148, v185, v100, v148
	v_fma_f32 v152, v186, v104, v152
	v_fma_f32 v156, v187, v108, v156
	v_fma_f32 v145, v184, v97, v145
	v_fma_f32 v149, v185, v101, v149
	v_fma_f32 v153, v186, v105, v153
	v_fma_f32 v157, v187, v109, v157
	v_fma_f32 v146, v184, v98, v146
	v_fma_f32 v150, v185, v102, v150
	v_fma_f32 v154, v186, v106, v154
	v_fma_f32 v158, v187, v110, v158
	v_fma_f32 v147, v184, v99, v147
	v_fma_f32 v151, v185, v103, v151
	v_fma_f32 v155, v186, v107, v155
	v_fma_f32 v159, v187, v111, v159
	v_cvt_pk_bf16_f32 v178, v144, v145
	v_cvt_pk_bf16_f32 v179, v146, v147
	v_cvt_pk_bf16_f32 v180, v148, v149
	v_cvt_pk_bf16_f32 v181, v150, v151
	v_cvt_pk_bf16_f32 v182, v152, v153
	v_cvt_pk_bf16_f32 v183, v154, v155
	v_cvt_pk_bf16_f32 v184, v156, v157
	v_cvt_pk_bf16_f32 v185, v158, v159
	global_store_dword v209, v178, s[44:45]
	global_store_dword v209, v179, s[44:45] offset:256
	global_store_dword v209, v180, s[44:45] offset:512
	global_store_dword v209, v181, s[44:45] offset:768
	global_store_dword v209, v182, s[44:45] offset:1024
	global_store_dword v209, v183, s[44:45] offset:1280
	global_store_dword v209, v184, s[44:45] offset:1536
	global_store_dword v209, v185, s[44:45] offset:1792
	s_add_i32 s13, s13, 1
	s_add_i32 s60, s60, -1
	s_cmp_lg_u32 s60, 0
	s_cbranch_scc1 .Lmylru_loop_0
	s_lshl_b32 s50, s10, 10
	s_lshl_b32 s51, s11, 6
	s_add_i32 s50, s50, s51
	s_lshl_b32 s51, s8, 4
	s_add_i32 s50, s50, s51
	s_add_i32 s50, s50, 512
	s_lshl_b32 s50, s50, 9
	s_add_u32 s46, s2, s50
	s_addc_u32 s47, s3, 0
	s_add_u32 s46, s46, 0x1000000
	s_addc_u32 s47, s47, 0
	s_add_u32 s48, s46, 0x20000
	s_addc_u32 s49, s47, 0
	v_lshlrev_b32_e32 v178, 9, v160
	v_lshl_add_u32 v178, v161, 4, v178
	global_load_dwordx4 v[0:3], v178, s[46:47]
	global_load_dwordx4 v[4:7], v178, s[46:47] offset:64
	global_load_dwordx4 v[8:11], v178, s[46:47] offset:128
	global_load_dwordx4 v[12:15], v178, s[46:47] offset:192
	global_load_dwordx4 v[16:19], v178, s[46:47] offset:256
	global_load_dwordx4 v[20:23], v178, s[46:47] offset:320
	global_load_dwordx4 v[24:27], v178, s[46:47] offset:384
	global_load_dwordx4 v[28:31], v178, s[46:47] offset:448
	global_load_dwordx4 v[32:35], v178, s[48:49]
	global_load_dwordx4 v[36:39], v178, s[48:49] offset:64
	global_load_dwordx4 v[40:43], v178, s[48:49] offset:128
	global_load_dwordx4 v[44:47], v178, s[48:49] offset:192
	global_load_dwordx4 v[48:51], v178, s[48:49] offset:256
	global_load_dwordx4 v[52:55], v178, s[48:49] offset:320
	global_load_dwordx4 v[56:59], v178, s[48:49] offset:384
	global_load_dwordx4 v[60:63], v178, s[48:49] offset:448
	s_load_dwordx2 s[46:47], s[0:1], 0xc8
	s_load_dwordx2 s[48:49], s[0:1], 0xd8
	s_load_dwordx2 s[40:41], s[0:1], 0xe0
	s_lshl_b32 s50, s10, 8
	s_lshl_b32 s51, s11, 6
	s_add_i32 s50, s50, s51
	s_lshl_b32 s51, s8, 4
	s_add_i32 s50, s50, s51
	v_add_u32_e32 v179, s50, v160
	v_lshlrev_b32_e32 v179, 2, v179
	s_waitcnt lgkmcnt(0)
	global_load_dword v173, v179, s[46:47]
	global_load_dword v174, v179, s[48:49]
	global_load_dword v175, v179, s[40:41]
	v_cmp_gt_u32_e64 s[34:35], 48, v202
	v_cmp_gt_u32_e64 s[36:37], 32, v202
	v_add_u32_e32 v204, 16, v202
	v_add_u32_e32 v205, 32, v202
	v_mov_b32_e32 v206, v160
	s_cmp_eq_u32 s7, 0
	s_cselect_b64 s[38:39], -1, 0
	v_and_b32_e32 v204, 63, v204
	v_lshlrev_b32_e32 v204, 2, v204
	v_and_b32_e32 v205, 63, v205
	v_lshlrev_b32_e32 v205, 2, v205
	v_and_b32_e32 v206, 63, v206
	v_lshlrev_b32_e32 v206, 2, v206
	v_mov_b32_e32 v176, 0
	s_mov_b32 s53, 0xbfb8aa3b
	s_waitcnt vmcnt(0)
	v_mul_f32_e32 v173, s53, v173
	v_mul_f32_e32 v174, s53, v174
	v_mul_f32_e32 v175, s53, v175
	v_exp_f32_e32 v175, v175
	s_nop 0
	v_add_f32_e32 v180, 1.0, v175
	v_log_f32_e32 v180, v180
	v_mov_b32_e32 v181, 0x3eaaaaab
	v_fma_f32 v181, v175, v181, -0.5
	v_fma_f32 v181, v175, v181, 1.0
	v_mul_f32_e32 v181, v175, v181
	v_mul_f32_e32 v181, 0x3fb8aa3b, v181
	v_cmp_gt_f32_e32 vcc, 0x3cf5c28f, v175
	s_nop 1
	v_cndmask_b32_e32 v175, v180, v181, vcc
	v_mul_f32_e32 v175, 0xc1000000, v175
	s_mov_b32 s13, 0
	s_barrier
	s_cmp_lt_u32 s13, 2
	s_sub_i32 s50, 1, s13
	s_lshl_b32 s50, s50, 7
	s_lshl_b32 s51, s9, 8
	s_add_i32 s51, s51, 0x8000
	s_add_i32 s51, s51, s50
	s_sub_i32 s50, 17, s13
	s_lshl_b32 s50, s50, 7
	s_lshl_b32 s59, s9, 11
	s_add_i32 s59, s59, s50
	s_cmp_lt_u32 s13, 2
	s_cselect_b32 s59, s51, s59
	s_lshl_b32 s52, s59, 11
	s_add_u32 s46, s16, s52
	s_addc_u32 s47, s17, 0
	s_lshl_b32 s52, s6, 13
	s_mov_b32 m0, s52
	s_add_i32 s52, s52, 0x400
	global_load_lds_dwordx4 v211, s[46:47]
	s_mov_b32 m0, s52
	s_add_i32 s52, s52, 0x400
	global_load_lds_dwordx4 v212, s[46:47]
	s_mov_b32 m0, s52
	s_add_i32 s52, s52, 0x400
	global_load_lds_dwordx4 v213, s[46:47]
	s_mov_b32 m0, s52
	s_add_i32 s52, s52, 0x400
	global_load_lds_dwordx4 v214, s[46:47]
	s_mov_b32 m0, s52
	s_add_i32 s52, s52, 0x400
	global_load_lds_dwordx4 v215, s[46:47]
	s_mov_b32 m0, s52
	s_add_i32 s52, s52, 0x400
	global_load_lds_dwordx4 v216, s[46:47]
	s_mov_b32 m0, s52
	s_add_i32 s52, s52, 0x400
	global_load_lds_dwordx4 v217, s[46:47]
	s_mov_b32 m0, s52
	s_nop 0
	global_load_lds_dwordx4 v218, s[46:47]
	s_waitcnt vmcnt(0)
	s_barrier
	s_cmp_gt_u32 s13, 15
	s_cbranch_scc1 .Lmylru_nopf_5
	s_add_i32 s58, s13, 2
	s_cmp_lt_u32 s58, 2
	s_sub_i32 s50, 1, s58
	s_lshl_b32 s50, s50, 7
	s_lshl_b32 s51, s9, 8
	s_add_i32 s51, s51, 0x8000
	s_add_i32 s51, s51, s50
	s_sub_i32 s50, 17, s58
	s_lshl_b32 s50, s50, 7
	s_lshl_b32 s59, s9, 11
	s_add_i32 s59, s59, s50
	s_cmp_lt_u32 s58, 2
	s_cselect_b32 s59, s51, s59
	s_lshl_b32 s52, s59, 11
	s_add_u32 s46, s16, s52
	s_addc_u32 s47, s17, 0
	s_lshl_b32 s52, s6, 10
	s_add_i32 s52, s52, 0x24800
	s_mov_b32 m0, s52
	s_nop 0
	global_load_lds_dwordx4 v169, s[46:47]
.Lmylru_nopf_5:
	s_cmp_eq_u32 s13, 17
	s_cbranch_scc1 .Lmylru_nodma_5
	s_add_i32 s58, s13, 1
	s_cmp_lt_u32 s58, 2
	s_sub_i32 s50, 1, s58
	s_lshl_b32 s50, s50, 7
	s_lshl_b32 s51, s9, 8
	s_add_i32 s51, s51, 0x8000
	s_add_i32 s51, s51, s50
	s_sub_i32 s50, 17, s58
	s_lshl_b32 s50, s50, 7
	s_lshl_b32 s59, s9, 11
	s_add_i32 s59, s59, s50
	s_cmp_lt_u32 s58, 2
	s_cselect_b32 s59, s51, s59
	s_lshl_b32 s52, s59, 11
	s_add_u32 s46, s16, s52
	s_addc_u32 s47, s17, 0
	s_lshl_b32 s52, s6, 13
	s_add_i32 s52, s52, 0x10000
	s_mov_b32 m0, s52
	s_add_i32 s52, s52, 0x400
	global_load_lds_dwordx4 v211, s[46:47]
	s_mov_b32 m0, s52
	s_add_i32 s52, s52, 0x400
	global_load_lds_dwordx4 v212, s[46:47]
	s_mov_b32 m0, s52
	s_add_i32 s52, s52, 0x400
	global_load_lds_dwordx4 v213, s[46:47]
	s_mov_b32 m0, s52
	s_add_i32 s52, s52, 0x400
	global_load_lds_dwordx4 v214, s[46:47]
	s_mov_b32 m0, s52
	s_add_i32 s52, s52, 0x400
	global_load_lds_dwordx4 v215, s[46:47]
	s_mov_b32 m0, s52
	s_add_i32 s52, s52, 0x400
	global_load_lds_dwordx4 v216, s[46:47]
	s_mov_b32 m0, s52
	s_add_i32 s52, s52, 0x400
	global_load_lds_dwordx4 v217, s[46:47]
	s_mov_b32 m0, s52
	s_nop 0
	global_load_lds_dwordx4 v218, s[46:47]
.Lmylru_nodma_5:
	v_mov_b32_e32 v163, v162
	ds_read_b128 v[96:99], v163
	ds_read_b128 v[100:103], v163 offset:8192
	ds_read_b128 v[104:107], v163 offset:16384
	ds_read_b128 v[108:111], v163 offset:24576
	v_xor_b32_e32 v164, 0x40, v163
	ds_read_b128 v[112:115], v164
	ds_read_b128 v[116:119], v164 offset:8192
	ds_read_b128 v[120:123], v164 offset:16384
	ds_read_b128 v[124:127], v164 offset:24576
	s_waitcnt lgkmcnt(7)
	v_mfma_f32_16x16x32_bf16 v[64:67], v[96:99], v[0:3], 0
	v_mfma_f32_16x16x32_bf16 v[68:71], v[96:99], v[32:35], 0
	v_xor_b32_e32 v164, 0x80, v163
	ds_read_b128 v[96:99], v164
	s_waitcnt lgkmcnt(7)
	v_mfma_f32_16x16x32_bf16 v[72:75], v[100:103], v[0:3], 0
	v_mfma_f32_16x16x32_bf16 v[76:79], v[100:103], v[32:35], 0
	ds_read_b128 v[100:103], v164 offset:8192
	s_waitcnt lgkmcnt(7)
	v_mfma_f32_16x16x32_bf16 v[80:83], v[104:107], v[0:3], 0
	v_mfma_f32_16x16x32_bf16 v[84:87], v[104:107], v[32:35], 0
	ds_read_b128 v[104:107], v164 offset:16384
	s_waitcnt lgkmcnt(7)
	v_mfma_f32_16x16x32_bf16 v[88:91], v[108:111], v[0:3], 0
	v_mfma_f32_16x16x32_bf16 v[92:95], v[108:111], v[32:35], 0
	ds_read_b128 v[108:111], v164 offset:24576
	s_waitcnt lgkmcnt(7)
	v_mfma_f32_16x16x32_bf16 v[64:67], v[112:115], v[4:7], v[64:67]
	v_mfma_f32_16x16x32_bf16 v[68:71], v[112:115], v[36:39], v[68:71]
	v_xor_b32_e32 v164, 0xc0, v163
	ds_read_b128 v[112:115], v164
	s_waitcnt lgkmcnt(7)
	v_mfma_f32_16x16x32_bf16 v[72:75], v[116:119], v[4:7], v[72:75]
	v_mfma_f32_16x16x32_bf16 v[76:79], v[116:119], v[36:39], v[76:79]
	ds_read_b128 v[116:119], v164 offset:8192
	s_waitcnt lgkmcnt(7)
	v_mfma_f32_16x16x32_bf16 v[80:83], v[120:123], v[4:7], v[80:83]
	v_mfma_f32_16x16x32_bf16 v[84:87], v[120:123], v[36:39], v[84:87]
	ds_read_b128 v[120:123], v164 offset:16384
	s_waitcnt lgkmcnt(7)
	v_mfma_f32_16x16x32_bf16 v[88:91], v[124:127], v[4:7], v[88:91]
	v_mfma_f32_16x16x32_bf16 v[92:95], v[124:127], v[36:39], v[92:95]
	ds_read_b128 v[124:127], v164 offset:24576
	s_waitcnt lgkmcnt(7)
	v_mfma_f32_16x16x32_bf16 v[64:67], v[96:99], v[8:11], v[64:67]
	v_mfma_f32_16x16x32_bf16 v[68:71], v[96:99], v[40:43], v[68:71]
	v_xor_b32_e32 v164, 0x100, v163
	ds_read_b128 v[96:99], v164
	s_waitcnt lgkmcnt(7)
	v_mfma_f32_16x16x32_bf16 v[72:75], v[100:103], v[8:11], v[72:75]
	v_mfma_f32_16x16x32_bf16 v[76:79], v[100:103], v[40:43], v[76:79]
	ds_read_b128 v[100:103], v164 offset:8192
	s_waitcnt lgkmcnt(7)
	v_mfma_f32_16x16x32_bf16 v[80:83], v[104:107], v[8:11], v[80:83]
	v_mfma_f32_16x16x32_bf16 v[84:87], v[104:107], v[40:43], v[84:87]
	ds_read_b128 v[104:107], v164 offset:16384
	s_waitcnt lgkmcnt(7)
	v_mfma_f32_16x16x32_bf16 v[88:91], v[108:111], v[8:11], v[88:91]
	v_mfma_f32_16x16x32_bf16 v[92:95], v[108:111], v[40:43], v[92:95]
	ds_read_b128 v[108:111], v164 offset:24576
	s_waitcnt lgkmcnt(7)
	v_mfma_f32_16x16x32_bf16 v[64:67], v[112:115], v[12:15], v[64:67]
	v_mfma_f32_16x16x32_bf16 v[68:71], v[112:115], v[44:47], v[68:71]
	v_xor_b32_e32 v164, 0x140, v163
	ds_read_b128 v[112:115], v164
	s_waitcnt lgkmcnt(7)
	v_mfma_f32_16x16x32_bf16 v[72:75], v[116:119], v[12:15], v[72:75]
	v_mfma_f32_16x16x32_bf16 v[76:79], v[116:119], v[44:47], v[76:79]
	ds_read_b128 v[116:119], v164 offset:8192
	s_waitcnt lgkmcnt(7)
	v_mfma_f32_16x16x32_bf16 v[80:83], v[120:123], v[12:15], v[80:83]
	v_mfma_f32_16x16x32_bf16 v[84:87], v[120:123], v[44:47], v[84:87]
	ds_read_b128 v[120:123], v164 offset:16384
	s_waitcnt lgkmcnt(7)
	v_mfma_f32_16x16x32_bf16 v[88:91], v[124:127], v[12:15], v[88:91]
	v_mfma_f32_16x16x32_bf16 v[92:95], v[124:127], v[44:47], v[92:95]
	ds_read_b128 v[124:127], v164 offset:24576
	s_waitcnt lgkmcnt(7)
	v_mfma_f32_16x16x32_bf16 v[64:67], v[96:99], v[16:19], v[64:67]
	v_mfma_f32_16x16x32_bf16 v[68:71], v[96:99], v[48:51], v[68:71]
	v_xor_b32_e32 v164, 0x180, v163
	ds_read_b128 v[96:99], v164
	s_waitcnt lgkmcnt(7)
	v_mfma_f32_16x16x32_bf16 v[72:75], v[100:103], v[16:19], v[72:75]
	v_mfma_f32_16x16x32_bf16 v[76:79], v[100:103], v[48:51], v[76:79]
	ds_read_b128 v[100:103], v164 offset:8192
	s_waitcnt lgkmcnt(7)
	v_mfma_f32_16x16x32_bf16 v[80:83], v[104:107], v[16:19], v[80:83]
	v_mfma_f32_16x16x32_bf16 v[84:87], v[104:107], v[48:51], v[84:87]
	ds_read_b128 v[104:107], v164 offset:16384
	s_waitcnt lgkmcnt(7)
	v_mfma_f32_16x16x32_bf16 v[88:91], v[108:111], v[16:19], v[88:91]
	v_mfma_f32_16x16x32_bf16 v[92:95], v[108:111], v[48:51], v[92:95]
	ds_read_b128 v[108:111], v164 offset:24576
	s_waitcnt lgkmcnt(7)
	v_mfma_f32_16x16x32_bf16 v[64:67], v[112:115], v[20:23], v[64:67]
	v_mfma_f32_16x16x32_bf16 v[68:71], v[112:115], v[52:55], v[68:71]
	v_xor_b32_e32 v164, 0x1c0, v163
	ds_read_b128 v[112:115], v164
	s_waitcnt lgkmcnt(7)
	v_mfma_f32_16x16x32_bf16 v[72:75], v[116:119], v[20:23], v[72:75]
	v_mfma_f32_16x16x32_bf16 v[76:79], v[116:119], v[52:55], v[76:79]
	ds_read_b128 v[116:119], v164 offset:8192
	s_waitcnt lgkmcnt(7)
	v_mfma_f32_16x16x32_bf16 v[80:83], v[120:123], v[20:23], v[80:83]
	v_mfma_f32_16x16x32_bf16 v[84:87], v[120:123], v[52:55], v[84:87]
	ds_read_b128 v[120:123], v164 offset:16384
	s_waitcnt lgkmcnt(7)
	v_mfma_f32_16x16x32_bf16 v[88:91], v[124:127], v[20:23], v[88:91]
	v_mfma_f32_16x16x32_bf16 v[92:95], v[124:127], v[52:55], v[92:95]
	ds_read_b128 v[124:127], v164 offset:24576
	s_waitcnt lgkmcnt(7)
	v_mfma_f32_16x16x32_bf16 v[64:67], v[96:99], v[24:27], v[64:67]
	v_mfma_f32_16x16x32_bf16 v[68:71], v[96:99], v[56:59], v[68:71]
	s_waitcnt lgkmcnt(6)
	v_mfma_f32_16x16x32_bf16 v[72:75], v[100:103], v[24:27], v[72:75]
	v_mfma_f32_16x16x32_bf16 v[76:79], v[100:103], v[56:59], v[76:79]
	s_waitcnt lgkmcnt(5)
	v_mfma_f32_16x16x32_bf16 v[80:83], v[104:107], v[24:27], v[80:83]
	v_mfma_f32_16x16x32_bf16 v[84:87], v[104:107], v[56:59], v[84:87]
	s_waitcnt lgkmcnt(4)
	v_mfma_f32_16x16x32_bf16 v[88:91], v[108:111], v[24:27], v[88:91]
	v_mfma_f32_16x16x32_bf16 v[92:95], v[108:111], v[56:59], v[92:95]
	s_waitcnt lgkmcnt(3)
	v_mfma_f32_16x16x32_bf16 v[64:67], v[112:115], v[28:31], v[64:67]
	v_mfma_f32_16x16x32_bf16 v[68:71], v[112:115], v[60:63], v[68:71]
	s_waitcnt lgkmcnt(2)
	v_mfma_f32_16x16x32_bf16 v[72:75], v[116:119], v[28:31], v[72:75]
	v_mfma_f32_16x16x32_bf16 v[76:79], v[116:119], v[60:63], v[76:79]
	s_waitcnt lgkmcnt(1)
	v_mfma_f32_16x16x32_bf16 v[80:83], v[120:123], v[28:31], v[80:83]
	v_mfma_f32_16x16x32_bf16 v[84:87], v[120:123], v[60:63], v[84:87]
	s_waitcnt lgkmcnt(0)
	v_mfma_f32_16x16x32_bf16 v[88:91], v[124:127], v[28:31], v[88:91]
	v_mfma_f32_16x16x32_bf16 v[92:95], v[124:127], v[60:63], v[92:95]
	v_mov_b32_e32 v198, v165
	v_mov_b32_e32 v199, v166
	v_mov_b32_e32 v200, v167
	v_mov_b32_e32 v201, v168
	ds_read_u16 v144, v198
	ds_read_u16 v145, v199
	ds_read_u16 v146, v200
	ds_read_u16 v147, v201
	ds_read_u16 v148, v198 offset:8192
	ds_read_u16 v149, v199 offset:8192
	ds_read_u16 v150, v200 offset:8192
	ds_read_u16 v151, v201 offset:8192
	ds_read_u16 v152, v198 offset:16384
	ds_read_u16 v153, v199 offset:16384
	ds_read_u16 v154, v200 offset:16384
	ds_read_u16 v155, v201 offset:16384
	ds_read_u16 v156, v198 offset:24576
	ds_read_u16 v157, v199 offset:24576
	ds_read_u16 v158, v200 offset:24576
	ds_read_u16 v159, v201 offset:24576
	s_nop 7
	v_fma_f32 v178, v64, s53, v173
	v_fma_f32 v179, v65, s53, v173
	v_fma_f32 v180, v66, s53, v173
	v_fma_f32 v181, v67, s53, v173
	v_fma_f32 v182, v72, s53, v173
	v_fma_f32 v183, v73, s53, v173
	v_fma_f32 v184, v74, s53, v173
	v_fma_f32 v185, v75, s53, v173
	v_fma_f32 v186, v68, s53, v174
	v_fma_f32 v187, v69, s53, v174
	v_fma_f32 v188, v70, s53, v174
	v_fma_f32 v189, v71, s53, v174
	v_fma_f32 v190, v76, s53, v174
	v_fma_f32 v191, v77, s53, v174
	v_fma_f32 v192, v78, s53, v174
	v_fma_f32 v193, v79, s53, v174
	v_exp_f32_e32 v178, v178
	v_exp_f32_e32 v179, v179
	v_exp_f32_e32 v180, v180
	v_exp_f32_e32 v181, v181
	v_exp_f32_e32 v182, v182
	v_exp_f32_e32 v183, v183
	v_exp_f32_e32 v184, v184
	v_exp_f32_e32 v185, v185
	v_exp_f32_e32 v186, v186
	v_exp_f32_e32 v187, v187
	v_exp_f32_e32 v188, v188
	v_exp_f32_e32 v189, v189
	v_exp_f32_e32 v190, v190
	v_exp_f32_e32 v191, v191
	v_exp_f32_e32 v192, v192
	v_exp_f32_e32 v193, v193
	v_add_f32_e32 v178, 1.0, v178
	v_add_f32_e32 v179, 1.0, v179
	v_add_f32_e32 v180, 1.0, v180
	v_add_f32_e32 v181, 1.0, v181
	v_add_f32_e32 v182, 1.0, v182
	v_add_f32_e32 v183, 1.0, v183
	v_add_f32_e32 v184, 1.0, v184
	v_add_f32_e32 v185, 1.0, v185
	v_add_f32_e32 v186, 1.0, v186
	v_add_f32_e32 v187, 1.0, v187
	v_add_f32_e32 v188, 1.0, v188
	v_add_f32_e32 v189, 1.0, v189
	v_add_f32_e32 v190, 1.0, v190
	v_add_f32_e32 v191, 1.0, v191
	v_add_f32_e32 v192, 1.0, v192
	v_add_f32_e32 v193, 1.0, v193
	v_rcp_f32_e32 v178, v178
	v_rcp_f32_e32 v179, v179
	v_rcp_f32_e32 v180, v180
	v_rcp_f32_e32 v181, v181
	v_rcp_f32_e32 v182, v182
	v_rcp_f32_e32 v183, v183
	v_rcp_f32_e32 v184, v184
	v_rcp_f32_e32 v185, v185
	v_rcp_f32_e32 v186, v186
	v_rcp_f32_e32 v187, v187
	v_rcp_f32_e32 v188, v188
	v_rcp_f32_e32 v189, v189
	v_rcp_f32_e32 v190, v190
	v_rcp_f32_e32 v191, v191
	v_rcp_f32_e32 v192, v192
	v_rcp_f32_e32 v193, v193
	v_mul_f32_e32 v178, v175, v178
	v_mul_f32_e32 v179, v175, v179
	v_mul_f32_e32 v180, v175, v180
	v_mul_f32_e32 v181, v175, v181
	v_mul_f32_e32 v182, v175, v182
	v_mul_f32_e32 v183, v175, v183
	v_mul_f32_e32 v184, v175, v184
	v_mul_f32_e32 v185, v175, v185
	v_exp_f32_e32 v96, v178
	v_exp_f32_e32 v97, v179
	v_exp_f32_e32 v98, v180
	v_exp_f32_e32 v99, v181
	v_exp_f32_e32 v100, v182
	v_exp_f32_e32 v101, v183
	v_exp_f32_e32 v102, v184
	v_exp_f32_e32 v103, v185
	s_nop 0
	v_fma_f32 v194, -v96, v96, 1.0
	v_fma_f32 v195, -v97, v97, 1.0
	v_fma_f32 v196, -v98, v98, 1.0
	v_fma_f32 v197, -v99, v99, 1.0
	v_fma_f32 v198, -v100, v100, 1.0
	v_fma_f32 v199, -v101, v101, 1.0
	v_fma_f32 v200, -v102, v102, 1.0
	v_fma_f32 v201, -v103, v103, 1.0
	v_max_f32_e32 v194, 0, v194
	v_max_f32_e32 v195, 0, v195
	v_max_f32_e32 v196, 0, v196
	v_max_f32_e32 v197, 0, v197
	v_max_f32_e32 v198, 0, v198
	v_max_f32_e32 v199, 0, v199
	v_max_f32_e32 v200, 0, v200
	v_max_f32_e32 v201, 0, v201
	v_sqrt_f32_e32 v194, v194
	v_sqrt_f32_e32 v195, v195
	v_sqrt_f32_e32 v196, v196
	v_sqrt_f32_e32 v197, v197
	v_sqrt_f32_e32 v198, v198
	v_sqrt_f32_e32 v199, v199
	v_sqrt_f32_e32 v200, v200
	v_sqrt_f32_e32 v201, v201
	s_waitcnt lgkmcnt(8)
	v_lshlrev_b32_e32 v144, 16, v144
	v_lshlrev_b32_e32 v145, 16, v145
	v_lshlrev_b32_e32 v146, 16, v146
	v_lshlrev_b32_e32 v147, 16, v147
	v_lshlrev_b32_e32 v148, 16, v148
	v_lshlrev_b32_e32 v149, 16, v149
	v_lshlrev_b32_e32 v150, 16, v150
	v_lshlrev_b32_e32 v151, 16, v151
	v_mul_f32_e32 v194, v194, v186
	v_mul_f32_e32 v195, v195, v187
	v_mul_f32_e32 v196, v196, v188
	v_mul_f32_e32 v197, v197, v189
	v_mul_f32_e32 v198, v198, v190
	v_mul_f32_e32 v199, v199, v191
	v_mul_f32_e32 v200, v200, v192
	v_mul_f32_e32 v201, v201, v193
	v_mul_f32_e32 v144, v194, v144
	v_mul_f32_e32 v145, v195, v145
	v_mul_f32_e32 v146, v196, v146
	v_mul_f32_e32 v147, v197, v147
	v_mul_f32_e32 v148, v198, v148
	v_mul_f32_e32 v149, v199, v149
	v_mul_f32_e32 v150, v200, v150
	v_mul_f32_e32 v151, v201, v151
	v_fma_f32 v178, v80, s53, v173
	v_fma_f32 v179, v81, s53, v173
	v_fma_f32 v180, v82, s53, v173
	v_fma_f32 v181, v83, s53, v173
	v_fma_f32 v182, v88, s53, v173
	v_fma_f32 v183, v89, s53, v173
	v_fma_f32 v184, v90, s53, v173
	v_fma_f32 v185, v91, s53, v173
	v_fma_f32 v186, v84, s53, v174
	v_fma_f32 v187, v85, s53, v174
	v_fma_f32 v188, v86, s53, v174
	v_fma_f32 v189, v87, s53, v174
	v_fma_f32 v190, v92, s53, v174
	v_fma_f32 v191, v93, s53, v174
	v_fma_f32 v192, v94, s53, v174
	v_fma_f32 v193, v95, s53, v174
	v_exp_f32_e32 v178, v178
	v_exp_f32_e32 v179, v179
	v_exp_f32_e32 v180, v180
	v_exp_f32_e32 v181, v181
	v_exp_f32_e32 v182, v182
	v_exp_f32_e32 v183, v183
	v_exp_f32_e32 v184, v184
	v_exp_f32_e32 v185, v185
	v_exp_f32_e32 v186, v186
	v_exp_f32_e32 v187, v187
	v_exp_f32_e32 v188, v188
	v_exp_f32_e32 v189, v189
	v_exp_f32_e32 v190, v190
	v_exp_f32_e32 v191, v191
	v_exp_f32_e32 v192, v192
	v_exp_f32_e32 v193, v193
	v_add_f32_e32 v178, 1.0, v178
	v_add_f32_e32 v179, 1.0, v179
	v_add_f32_e32 v180, 1.0, v180
	v_add_f32_e32 v181, 1.0, v181
	v_add_f32_e32 v182, 1.0, v182
	v_add_f32_e32 v183, 1.0, v183
	v_add_f32_e32 v184, 1.0, v184
	v_add_f32_e32 v185, 1.0, v185
	v_add_f32_e32 v186, 1.0, v186
	v_add_f32_e32 v187, 1.0, v187
	v_add_f32_e32 v188, 1.0, v188
	v_add_f32_e32 v189, 1.0, v189
	v_add_f32_e32 v190, 1.0, v190
	v_add_f32_e32 v191, 1.0, v191
	v_add_f32_e32 v192, 1.0, v192
	v_add_f32_e32 v193, 1.0, v193
	v_rcp_f32_e32 v178, v178
	v_rcp_f32_e32 v179, v179
	v_rcp_f32_e32 v180, v180
	v_rcp_f32_e32 v181, v181
	v_rcp_f32_e32 v182, v182
	v_rcp_f32_e32 v183, v183
	v_rcp_f32_e32 v184, v184
	v_rcp_f32_e32 v185, v185
	v_rcp_f32_e32 v186, v186
	v_rcp_f32_e32 v187, v187
	v_rcp_f32_e32 v188, v188
	v_rcp_f32_e32 v189, v189
	v_rcp_f32_e32 v190, v190
	v_rcp_f32_e32 v191, v191
	v_rcp_f32_e32 v192, v192
	v_rcp_f32_e32 v193, v193
	v_mul_f32_e32 v178, v175, v178
	v_mul_f32_e32 v179, v175, v179
	v_mul_f32_e32 v180, v175, v180
	v_mul_f32_e32 v181, v175, v181
	v_mul_f32_e32 v182, v175, v182
	v_mul_f32_e32 v183, v175, v183
	v_mul_f32_e32 v184, v175, v184
	v_mul_f32_e32 v185, v175, v185
	v_exp_f32_e32 v104, v178
	v_exp_f32_e32 v105, v179
	v_exp_f32_e32 v106, v180
	v_exp_f32_e32 v107, v181
	v_exp_f32_e32 v108, v182
	v_exp_f32_e32 v109, v183
	v_exp_f32_e32 v110, v184
	v_exp_f32_e32 v111, v185
	s_nop 0
	v_fma_f32 v194, -v104, v104, 1.0
	v_fma_f32 v195, -v105, v105, 1.0
	v_fma_f32 v196, -v106, v106, 1.0
	v_fma_f32 v197, -v107, v107, 1.0
	v_fma_f32 v198, -v108, v108, 1.0
	v_fma_f32 v199, -v109, v109, 1.0
	v_fma_f32 v200, -v110, v110, 1.0
	v_fma_f32 v201, -v111, v111, 1.0
	v_max_f32_e32 v194, 0, v194
	v_max_f32_e32 v195, 0, v195
	v_max_f32_e32 v196, 0, v196
	v_max_f32_e32 v197, 0, v197
	v_max_f32_e32 v198, 0, v198
	v_max_f32_e32 v199, 0, v199
	v_max_f32_e32 v200, 0, v200
	v_max_f32_e32 v201, 0, v201
	v_sqrt_f32_e32 v194, v194
	v_sqrt_f32_e32 v195, v195
	v_sqrt_f32_e32 v196, v196
	v_sqrt_f32_e32 v197, v197
	v_sqrt_f32_e32 v198, v198
	v_sqrt_f32_e32 v199, v199
	v_sqrt_f32_e32 v200, v200
	v_sqrt_f32_e32 v201, v201
	s_waitcnt lgkmcnt(0)
	v_lshlrev_b32_e32 v152, 16, v152
	v_lshlrev_b32_e32 v153, 16, v153
	v_lshlrev_b32_e32 v154, 16, v154
	v_lshlrev_b32_e32 v155, 16, v155
	v_lshlrev_b32_e32 v156, 16, v156
	v_lshlrev_b32_e32 v157, 16, v157
	v_lshlrev_b32_e32 v158, 16, v158
	v_lshlrev_b32_e32 v159, 16, v159
	v_mul_f32_e32 v194, v194, v186
	v_mul_f32_e32 v195, v195, v187
	v_mul_f32_e32 v196, v196, v188
	v_mul_f32_e32 v197, v197, v189
	v_mul_f32_e32 v198, v198, v190
	v_mul_f32_e32 v199, v199, v191
	v_mul_f32_e32 v200, v200, v192
	v_mul_f32_e32 v201, v201, v193
	v_mul_f32_e32 v152, v194, v152
	v_mul_f32_e32 v153, v195, v153
	v_mul_f32_e32 v154, v196, v154
	v_mul_f32_e32 v155, v197, v155
	v_mul_f32_e32 v156, v198, v156
	v_mul_f32_e32 v157, v199, v157
	v_mul_f32_e32 v158, v200, v158
	v_mul_f32_e32 v159, v201, v159
	v_fma_f32 v146, v98, v147, v146
	v_fma_f32 v150, v102, v151, v150
	v_fma_f32 v154, v106, v155, v154
	v_fma_f32 v158, v110, v159, v158
	v_mul_f32_e32 v98, v98, v99
	v_mul_f32_e32 v102, v102, v103
	v_mul_f32_e32 v106, v106, v107
	v_mul_f32_e32 v110, v110, v111
	v_fma_f32 v145, v97, v146, v145
	v_fma_f32 v149, v101, v150, v149
	v_fma_f32 v153, v105, v154, v153
	v_fma_f32 v157, v109, v158, v157
	v_mul_f32_e32 v97, v97, v98
	v_mul_f32_e32 v101, v101, v102
	v_mul_f32_e32 v105, v105, v106
	v_mul_f32_e32 v109, v109, v110
	v_fma_f32 v144, v96, v145, v144
	v_fma_f32 v148, v100, v149, v148
	v_fma_f32 v152, v104, v153, v152
	v_fma_f32 v156, v108, v157, v156
	v_mul_f32_e32 v96, v96, v97
	v_mul_f32_e32 v100, v100, v101
	v_mul_f32_e32 v104, v104, v105
	v_mul_f32_e32 v108, v108, v109
	ds_bpermute_b32 v178, v204, v96
	ds_bpermute_b32 v182, v204, v144
	ds_bpermute_b32 v179, v204, v100
	ds_bpermute_b32 v183, v204, v148
	ds_bpermute_b32 v180, v204, v104
	ds_bpermute_b32 v184, v204, v152
	ds_bpermute_b32 v181, v204, v108
	ds_bpermute_b32 v185, v204, v156
	s_waitcnt lgkmcnt(0)
	v_fma_f32 v186, v182, v96, v144
	v_cndmask_b32_e64 v178, 1.0, v178, s[34:35]
	v_fma_f32 v187, v183, v100, v148
	v_cndmask_b32_e64 v179, 1.0, v179, s[34:35]
	v_fma_f32 v188, v184, v104, v152
	v_cndmask_b32_e64 v180, 1.0, v180, s[34:35]
	v_fma_f32 v189, v185, v108, v156
	v_cndmask_b32_e64 v181, 1.0, v181, s[34:35]
	v_cndmask_b32_e64 v223, v144, v186, s[34:35]
	v_mul_f32_e32 v219, v96, v178
	v_cndmask_b32_e64 v224, v148, v187, s[34:35]
	v_mul_f32_e32 v220, v100, v179
	v_cndmask_b32_e64 v225, v152, v188, s[34:35]
	v_mul_f32_e32 v221, v104, v180
	v_cndmask_b32_e64 v226, v156, v189, s[34:35]
	v_mul_f32_e32 v222, v108, v181
	ds_bpermute_b32 v178, v205, v219
	ds_bpermute_b32 v182, v205, v223
	ds_bpermute_b32 v179, v205, v220
	ds_bpermute_b32 v183, v205, v224
	ds_bpermute_b32 v180, v205, v221
	ds_bpermute_b32 v184, v205, v225
	ds_bpermute_b32 v181, v205, v222
	ds_bpermute_b32 v185, v205, v226
	s_waitcnt lgkmcnt(0)
	v_fma_f32 v186, v182, v219, v223
	v_cndmask_b32_e64 v178, 1.0, v178, s[36:37]
	v_fma_f32 v187, v183, v220, v224
	v_cndmask_b32_e64 v179, 1.0, v179, s[36:37]
	v_fma_f32 v188, v184, v221, v225
	v_cndmask_b32_e64 v180, 1.0, v180, s[36:37]
	v_fma_f32 v189, v185, v222, v226
	v_cndmask_b32_e64 v181, 1.0, v181, s[36:37]
	v_cndmask_b32_e64 v223, v223, v186, s[36:37]
	v_mul_f32_e32 v219, v219, v178
	v_cndmask_b32_e64 v224, v224, v187, s[36:37]
	v_mul_f32_e32 v220, v220, v179
	v_cndmask_b32_e64 v225, v225, v188, s[36:37]
	v_mul_f32_e32 v221, v221, v180
	v_cndmask_b32_e64 v226, v226, v189, s[36:37]
	v_mul_f32_e32 v222, v222, v181
	ds_bpermute_b32 v227, v204, v219
	ds_bpermute_b32 v231, v204, v223
	ds_bpermute_b32 v235, v206, v219
	ds_bpermute_b32 v239, v206, v223
	ds_bpermute_b32 v228, v204, v220
	ds_bpermute_b32 v232, v204, v224
	ds_bpermute_b32 v236, v206, v220
	ds_bpermute_b32 v244, v206, v224
	ds_bpermute_b32 v229, v204, v221
	ds_bpermute_b32 v233, v204, v225
	ds_bpermute_b32 v237, v206, v221
	ds_bpermute_b32 v245, v206, v225
	ds_bpermute_b32 v230, v204, v222
	ds_bpermute_b32 v234, v204, v226
	ds_bpermute_b32 v238, v206, v222
	ds_bpermute_b32 v246, v206, v226
	s_waitcnt lgkmcnt(0)
	v_cndmask_b32_e64 v227, 1.0, v227, s[34:35]
	v_cndmask_b32_e64 v231, 0, v231, s[34:35]
	v_cndmask_b32_e64 v228, 1.0, v228, s[34:35]
	v_cndmask_b32_e64 v232, 0, v232, s[34:35]
	v_cndmask_b32_e64 v229, 1.0, v229, s[34:35]
	v_cndmask_b32_e64 v233, 0, v233, s[34:35]
	v_cndmask_b32_e64 v230, 1.0, v230, s[34:35]
	v_cndmask_b32_e64 v234, 0, v234, s[34:35]
	v_mov_b32_e32 v190, v238
	v_mov_b32_e32 v194, v246
	v_mov_b32_e32 v198, v190
	v_mov_b32_e32 v201, v194
	v_fma_f32 v194, v194, v237, v245
	v_mul_f32_e32 v190, v190, v237
	v_mov_b32_e32 v199, v190
	v_mov_b32_e32 v177, v194
	v_fma_f32 v194, v194, v236, v244
	v_mul_f32_e32 v190, v190, v236
	v_mov_b32_e32 v200, v190
	v_mov_b32_e32 v203, v194
	v_fma_f32 v194, v194, v235, v239
	v_mul_f32_e32 v190, v190, v235
	v_mov_b32_e32 v191, v194
	ds_write_b64 v207, v[190:191]
	s_waitcnt lgkmcnt(0)
	s_barrier
	ds_read_b64 v[178:179], v208 offset:512
	ds_read_b64 v[180:181], v208
	s_waitcnt lgkmcnt(0)
	v_fma_f32 v182, v176, v178, v179
	v_cndmask_b32_e64 v183, v176, v182, s[38:39]
	v_fma_f32 v176, v182, v180, v181
	s_add_i32 s13, s13, 1
	s_waitcnt vmcnt(0)
	s_barrier
	s_cmp_gt_u32 s13, 15
	s_cbranch_scc1 .Lmylru_nopf_6
	s_add_i32 s58, s13, 2
	s_cmp_lt_u32 s58, 2
	s_sub_i32 s50, 1, s58
	s_lshl_b32 s50, s50, 7
	s_lshl_b32 s51, s9, 8
	s_add_i32 s51, s51, 0x8000
	s_add_i32 s51, s51, s50
	s_sub_i32 s50, 17, s58
	s_lshl_b32 s50, s50, 7
	s_lshl_b32 s59, s9, 11
	s_add_i32 s59, s59, s50
	s_cmp_lt_u32 s58, 2
	s_cselect_b32 s59, s51, s59
	s_lshl_b32 s52, s59, 11
	s_add_u32 s46, s16, s52
	s_addc_u32 s47, s17, 0
	s_lshl_b32 s52, s6, 10
	s_add_i32 s52, s52, 0x24800
	s_mov_b32 m0, s52
	s_nop 0
	global_load_lds_dwordx4 v169, s[46:47]
.Lmylru_nopf_6:
	s_cmp_eq_u32 s13, 17
	s_cbranch_scc1 .Lmylru_nodma_6
	s_add_i32 s58, s13, 1
	s_cmp_lt_u32 s58, 2
	s_sub_i32 s50, 1, s58
	s_lshl_b32 s50, s50, 7
	s_lshl_b32 s51, s9, 8
	s_add_i32 s51, s51, 0x8000
	s_add_i32 s51, s51, s50
	s_sub_i32 s50, 17, s58
	s_lshl_b32 s50, s50, 7
	s_lshl_b32 s59, s9, 11
	s_add_i32 s59, s59, s50
	s_cmp_lt_u32 s58, 2
	s_cselect_b32 s59, s51, s59
	s_lshl_b32 s52, s59, 11
	s_add_u32 s46, s16, s52
	s_addc_u32 s47, s17, 0
	s_lshl_b32 s52, s6, 13
	s_mov_b32 m0, s52
	s_add_i32 s52, s52, 0x400
	global_load_lds_dwordx4 v211, s[46:47]
	s_mov_b32 m0, s52
	s_add_i32 s52, s52, 0x400
	global_load_lds_dwordx4 v212, s[46:47]
	s_mov_b32 m0, s52
	s_add_i32 s52, s52, 0x400
	global_load_lds_dwordx4 v213, s[46:47]
	s_mov_b32 m0, s52
	s_add_i32 s52, s52, 0x400
	global_load_lds_dwordx4 v214, s[46:47]
	s_mov_b32 m0, s52
	s_add_i32 s52, s52, 0x400
	global_load_lds_dwordx4 v215, s[46:47]
	s_mov_b32 m0, s52
	s_add_i32 s52, s52, 0x400
	global_load_lds_dwordx4 v216, s[46:47]
	s_mov_b32 m0, s52
	s_add_i32 s52, s52, 0x400
	global_load_lds_dwordx4 v217, s[46:47]
	s_mov_b32 m0, s52
	s_nop 0
	global_load_lds_dwordx4 v218, s[46:47]

.Lmylru_t1_7:
	s_barrier
	s_sub_i32 s54, 17, s13
	s_lshl_b32 s55, s54, 14
	s_lshl_b32 s56, s6, 11
	s_add_i32 s55, s55, s56
	s_add_u32 s44, s22, s55
	s_addc_u32 s45, s23, 0
	s_cmp_lt_u32 s13, 2
	s_sub_i32 s50, 1, s13
	s_lshl_b32 s50, s50, 7
	s_lshl_b32 s51, s9, 8
	s_add_i32 s51, s51, 0x8000
	s_add_i32 s51, s51, s50
	s_sub_i32 s50, 17, s13
	s_lshl_b32 s50, s50, 7
	s_lshl_b32 s57, s9, 11
	s_add_i32 s57, s57, s50
	s_cmp_lt_u32 s13, 2
	s_cselect_b32 s57, s51, s57
	s_lshl_b32 s57, s57, 11
	s_add_u32 s40, s18, s57
	s_addc_u32 s41, s19, 0
	s_add_u32 s42, s20, s57
	s_addc_u32 s43, s21, 0
	global_load_dword v247, v209, s[44:45]
	global_load_dword v248, v209, s[44:45] offset:256
	global_load_dword v249, v209, s[44:45] offset:512
	global_load_dword v250, v209, s[44:45] offset:768
	global_load_dword v251, v209, s[44:45] offset:1024
	global_load_dword v252, v209, s[44:45] offset:1280
	global_load_dword v253, v209, s[44:45] offset:1536
	global_load_dword v254, v209, s[44:45] offset:1792
	v_add_u32_e32 v182, 0x0, v210
	v_add_u32_e32 v183, 0x1000, v182
	global_load_ushort v128, v182, s[40:41]
	global_load_ushort v129, v182, s[40:41] offset:2048
	global_load_ushort v130, v183, s[40:41]
	global_load_ushort v131, v183, s[40:41] offset:2048
	v_add_u32_e32 v182, 0x8000, v210
	v_add_u32_e32 v183, 0x1000, v182
	global_load_ushort v132, v182, s[40:41]
	global_load_ushort v133, v182, s[40:41] offset:2048
	global_load_ushort v134, v183, s[40:41]
	global_load_ushort v135, v183, s[40:41] offset:2048
	v_add_u32_e32 v182, 0x10000, v210
	v_add_u32_e32 v183, 0x1000, v182
	global_load_ushort v136, v182, s[40:41]
	global_load_ushort v137, v182, s[40:41] offset:2048
	global_load_ushort v138, v183, s[40:41]
	global_load_ushort v139, v183, s[40:41] offset:2048
	v_add_u32_e32 v182, 0x18000, v210
	v_add_u32_e32 v183, 0x1000, v182
	global_load_ushort v140, v182, s[40:41]
	global_load_ushort v141, v182, s[40:41] offset:2048
	global_load_ushort v142, v183, s[40:41]
	global_load_ushort v143, v183, s[40:41] offset:2048
	s_cmp_gt_u32 s13, 15
	s_cbranch_scc1 .Lmylru_nopf_7
	s_add_i32 s58, s13, 2
	s_cmp_lt_u32 s58, 2
	s_sub_i32 s50, 1, s58
	s_lshl_b32 s50, s50, 7
	s_lshl_b32 s51, s9, 8
	s_add_i32 s51, s51, 0x8000
	s_add_i32 s51, s51, s50
	s_sub_i32 s50, 17, s58
	s_lshl_b32 s50, s50, 7
	s_lshl_b32 s59, s9, 11
	s_add_i32 s59, s59, s50
	s_cmp_lt_u32 s58, 2
	s_cselect_b32 s59, s51, s59
	s_lshl_b32 s52, s59, 11
	s_add_u32 s46, s16, s52
	s_addc_u32 s47, s17, 0
	s_lshl_b32 s52, s6, 10
	s_add_i32 s52, s52, 0x24800
	s_mov_b32 m0, s52
	s_nop 0
	global_load_lds_dwordx4 v169, s[46:47]
